# v51 + nt on GEMM-epilogue side loads and the remaining non-DMA loads of the GEMM-type phases
# baseline (speedup 1.0000x reference)
.LBB0_17:
	s_mov_b32 s86, s81
	s_mov_b32 s0, -1
	s_ashr_i32 s87, s86, 31
	s_waitcnt lgkmcnt(0)
	v_mbcnt_lo_u32_b32 v0, s0, 0
	v_mbcnt_hi_u32_b32 v0, s0, v0
	v_readlane_b32 s0, v250, 5
	s_nop 1
	v_add_u32_e32 v235, s0, v0
	s_nop 0
	v_readfirstlane_b32 s0, v235
	s_ashr_i32 s16, s0, 6
	s_mov_b32 s14, s16
	v_writelane_b32 v253, s0, 31
	v_writelane_b32 v253, s14, 32
	v_readlane_b32 s0, v250, 10
	s_add_i32 s30, s16, s0
	v_writelane_b32 v253, s15, 33
	v_and_b32_e32 v198, 63, v235
	v_readlane_b32 s36, v253, 16
	v_readlane_b32 s38, v253, 18
	v_readlane_b32 s39, v253, 19
	s_add_u32 s74, s38, s86
	s_addc_u32 s75, s39, s87
	s_lshl_b64 s[0:1], s[86:87], 2
	v_readlane_b32 s37, v253, 17
	s_add_u32 s14, s36, s0
	s_addc_u32 s15, s37, s1
	v_writelane_b32 v253, s14, 34
	s_cmp_lg_u32 s42, 0
	s_nop 0
	v_writelane_b32 v253, s15, 35
	v_writelane_b32 v253, s42, 36
	s_mov_b64 s[14:15], -1
	s_cbranch_scc0 .LBB0_577
	v_readlane_b32 s14, v253, 36
	s_cmp_lt_i32 s14, 1
	v_readlane_b32 s88, v253, 37
	s_cbranch_scc1 .LBB0_576
	v_readlane_b32 s16, v253, 36
	s_add_i32 s14, s16, -1
	s_lshr_b32 s15, s14, 1
	s_mul_hi_u32 s15, s15, 0x92492493
	s_lshr_b32 s15, s15, 2
	v_writelane_b32 v253, s15, 38
	s_mul_i32 s15, s15, 14
	s_sub_i32 s17, s14, s15
	s_cmp_lt_u32 s16, 15
	s_cselect_b64 s[14:15], -1, 0
	v_writelane_b32 v253, s14, 39
	s_cmp_gt_u32 s16, 14
	s_nop 0
	v_writelane_b32 v253, s15, 40
	s_cselect_b64 s[14:15], -1, 0
	v_writelane_b32 v253, s14, 41
	s_nop 1
	v_writelane_b32 v253, s15, 42
	s_add_u32 s14, s74, 0x10000
	v_writelane_b32 v253, s14, 43
	s_addc_u32 s14, s75, 0
	v_writelane_b32 v253, s14, 44
	v_writelane_b32 v253, s17, 45
	s_cmp_lt_i32 s17, 5
	s_mov_b64 s[14:15], -1
	s_cbranch_scc1 .LBB0_566
	v_readlane_b32 s14, v253, 45
	s_cmp_lt_i32 s14, 10
	s_mov_b64 s[14:15], -1
	s_cbranch_scc1 .LBB0_378
	v_readlane_b32 s14, v253, 45
	s_cmp_lt_i32 s14, 12
	s_mov_b64 s[14:15], -1
	s_cbranch_scc1 .LBB0_346
	v_readlane_b32 s14, v253, 45
	s_cmp_lt_i32 s14, 13
	s_mov_b64 s[14:15], -1
	s_cbranch_scc1 .LBB0_29
	v_readlane_b32 s14, v253, 45
	s_cmp_eq_u32 s14, 13
	s_cbranch_scc0 .LBB0_28
	v_readlane_b32 s14, v253, 36
	s_add_i32 s14, s14, -15
	s_cmp_gt_u32 s14, 13
	s_cbranch_scc1 .LBB0_28
	v_readlane_b32 s14, v252, 38
	v_readlane_b32 s15, v252, 39
	s_andn2_b64 vcc, exec, s[14:15]
	s_cbranch_vccnz .LBB0_28
	s_lshl_b64 s[14:15], s[86:87], 3
	v_readlane_b32 s16, v250, 3
	v_readlane_b32 s17, v250, 4
	s_add_u32 s14, s16, s14
	s_addc_u32 s15, s17, s15
	s_load_dwordx2 s[14:15], s[14:15], 0x98
	v_lshlrev_b32_e32 v0, 4, v198
	s_waitcnt vmcnt(0)
	v_lshlrev_b32_e32 v18, 3, v198
	s_waitcnt lgkmcnt(0)
	global_load_dwordx4 v[2:5], v0, s[14:15] offset:3072 nt
	global_load_dwordx4 v[6:9], v0, s[14:15] offset:2048 nt
	global_load_dwordx4 v[10:13], v0, s[14:15] offset:1024 nt
	global_load_dwordx4 v[14:17], v0, s[14:15] nt
	v_mov_b32_e32 v19, v1
	v_readlane_b32 s15, v252, 37
	v_lshl_add_u64 v[20:21], s[74:75], 0, v[18:19]
	s_mov_b64 s[16:17], 0x2200000
	s_mul_i32 s14, s15, s30
	v_lshl_add_u64 v[22:23], v[20:21], 0, s[16:17]
	v_readlane_b32 s16, v253, 34
	v_readlane_b32 s17, v253, 35
	s_add_i32 s31, s14, s15
	s_ashr_i32 s15, s14, 31
	v_lshl_add_u64 v[24:25], s[16:17], 0, v[0:1]
	s_lshl_b64 s[16:17], s[14:15], 11
	v_readlane_b32 s29, v253, 0
	s_add_u32 s16, s29, s16
	v_readlane_b32 s38, v253, 1
	s_addc_u32 s17, s38, s17
	v_lshl_add_u64 v[26:27], s[16:17], 0, v[18:19]
	s_add_i32 s16, s14, 2
	s_ashr_i32 s17, s16, 31
	s_lshl_b64 s[34:35], s[16:17], 12
	v_readlane_b32 s40, v253, 16
	v_readlane_b32 s41, v253, 17
	s_add_u32 s34, s40, s34
	s_addc_u32 s35, s41, s35
	v_lshl_add_u64 v[28:29], s[34:35], 0, v[0:1]
	s_lshl_b64 s[34:35], s[14:15], 12
	s_add_u32 s34, s40, s34
	s_addc_u32 s35, s41, s35
	v_readlane_b32 s42, v253, 18
	v_lshl_add_u64 v[30:31], s[34:35], 0, v[0:1]
	s_lshl_b64 s[34:35], s[14:15], 3
	v_readlane_b32 s43, v253, 19
	s_add_u32 s15, s42, s34
	s_addc_u32 s34, s43, s35
	s_lshl_b64 s[16:17], s[16:17], 11
	s_add_u32 s16, s29, s16
	s_addc_u32 s17, s38, s17
	v_lshl_add_u64 v[32:33], s[16:17], 0, v[18:19]
	s_add_i32 s16, s14, 1
	s_ashr_i32 s17, s16, 31
	s_lshl_b64 s[36:37], s[16:17], 12
	s_add_u32 s36, s40, s36
	s_addc_u32 s37, s41, s37
	s_lshl_b64 s[16:17], s[16:17], 11
	s_add_u32 s16, s29, s16
	s_addc_u32 s17, s38, s17
	v_lshl_add_u64 v[34:35], s[36:37], 0, v[0:1]
	v_lshl_add_u64 v[36:37], s[16:17], 0, v[18:19]
	s_mov_b64 s[38:39], 0x2000
	s_mov_b64 s[40:41], 0x4000
.LBB0_27:
	s_add_u32 s16, s15, s86
	s_addc_u32 s17, s34, s87
	s_add_u32 s36, s16, 0xd0000
	s_addc_u32 s37, s17, 0
	global_load_dwordx4 v[18:21], v1, s[36:37] offset:16 nt
	global_load_dwordx4 v[62:65], v228, s[16:17] nt
	v_lshl_add_u64 v[38:39], v[26:27], 0, s[86:87]
	global_load_dwordx2 v[68:69], v[38:39], off offset:-1024 nt
	global_load_dwordx2 v[70:71], v[38:39], off offset:-512 nt
	global_load_dwordx2 v[72:73], v[38:39], off nt
	global_load_dwordx2 v[74:75], v[38:39], off offset:512 nt
	v_lshl_add_u64 v[38:39], v[36:37], 0, s[86:87]
	global_load_dwordx2 v[60:61], v[38:39], off offset:-1024 nt
	global_load_dwordx2 v[58:59], v[38:39], off offset:-512 nt
	global_load_dwordx2 v[56:57], v[38:39], off nt
	global_load_dwordx2 v[54:55], v[38:39], off offset:512 nt
	v_lshl_add_u64 v[38:39], v[32:33], 0, s[86:87]
	global_load_dwordx2 v[52:53], v[38:39], off offset:-1024 nt
	global_load_dwordx2 v[50:51], v[38:39], off offset:-512 nt
	global_load_dwordx2 v[48:49], v[38:39], off nt
	global_load_dwordx2 v[46:47], v[38:39], off offset:512 nt
	s_add_i32 s16, s14, 3
	s_ashr_i32 s17, s16, 31
	s_lshl_b64 s[36:37], s[16:17], 11
	v_lshl_add_u64 v[38:39], v[22:23], 0, s[36:37]
	global_load_dwordx2 v[44:45], v[38:39], off nt
	global_load_dwordx2 v[42:43], v[38:39], off offset:512 nt
	global_load_dwordx2 v[40:41], v[38:39], off offset:1024 nt
	s_nop 0
	global_load_dwordx2 v[38:39], v[38:39], off offset:1536 nt
	s_lshl_b64 s[16:17], s[16:17], 12
	s_add_i32 s14, s14, 4
	s_add_u32 s15, s15, 32
	s_addc_u32 s34, s34, 0
	v_lshl_add_u64 v[26:27], v[26:27], 0, s[38:39]
	v_lshl_add_u64 v[32:33], v[32:33], 0, s[38:39]
	v_lshl_add_u64 v[36:37], v[36:37], 0, s[38:39]
	s_cmp_ge_i32 s14, s31
	s_waitcnt vmcnt(15)
	v_lshlrev_b32_e32 v66, 16, v68
	v_ffbh_u32_e32 v0, v63
	v_min_u32_e32 v0, 32, v0
	v_lshlrev_b64 v[62:63], v0, v[62:63]
	v_min_u32_e32 v62, 1, v62
	v_or_b32_e32 v62, v63, v62
	v_cvt_f32_u32_e32 v62, v62
	v_sub_u32_e32 v0, 32, v0
	v_and_b32_e32 v67, 0xffff0000, v68
	v_lshlrev_b32_e32 v68, 16, v69
	v_ldexp_f32 v0, v62, v0
	v_fmamk_f32 v0, v0, 0x32800000, v196
	v_cmp_gt_f32_e32 vcc, s96, v0
	v_mul_f32_e32 v62, 0x4b800000, v0
	v_and_b32_e32 v69, 0xffff0000, v69
	v_cndmask_b32_e32 v0, v0, v62, vcc
	v_rsq_f32_e32 v0, v0
	s_nop 0
	v_mul_f32_e32 v62, 0x45800000, v0
	v_cndmask_b32_e32 v0, v0, v62, vcc
	v_pk_mul_f32 v[66:67], v[0:1], v[66:67] op_sel_hi:[0,1]
	v_pk_mul_f32 v[68:69], v[0:1], v[68:69] op_sel_hi:[0,1]
	v_lshl_add_u64 v[62:63], v[30:31], 0, s[0:1]
	v_pk_mul_f32 v[66:67], v[14:15], v[66:67]
	v_pk_mul_f32 v[68:69], v[16:17], v[68:69]
	global_store_dwordx4 v[62:63], v[66:69], off sc1
	v_lshl_add_u64 v[30:31], v[30:31], 0, s[40:41]
	s_waitcnt vmcnt(15)
	v_lshlrev_b32_e32 v66, 16, v70
	v_and_b32_e32 v67, 0xffff0000, v70
	v_lshlrev_b32_e32 v68, 16, v71
	v_and_b32_e32 v69, 0xffff0000, v71
	v_pk_mul_f32 v[66:67], v[0:1], v[66:67] op_sel_hi:[0,1]
	v_pk_mul_f32 v[68:69], v[0:1], v[68:69] op_sel_hi:[0,1]
	v_pk_mul_f32 v[66:67], v[10:11], v[66:67]
	v_pk_mul_f32 v[68:69], v[12:13], v[68:69]
	global_store_dwordx4 v[62:63], v[66:69], off offset:1024 sc1
	s_waitcnt vmcnt(15)
	s_nop 0
	v_lshlrev_b32_e32 v66, 16, v72
	v_and_b32_e32 v67, 0xffff0000, v72
	v_lshlrev_b32_e32 v68, 16, v73
	v_and_b32_e32 v69, 0xffff0000, v73
	v_pk_mul_f32 v[66:67], v[0:1], v[66:67] op_sel_hi:[0,1]
	v_pk_mul_f32 v[68:69], v[0:1], v[68:69] op_sel_hi:[0,1]
	v_pk_mul_f32 v[66:67], v[6:7], v[66:67]
	v_pk_mul_f32 v[68:69], v[8:9], v[68:69]
	global_store_dwordx4 v[62:63], v[66:69], off offset:2048 sc1
	s_waitcnt vmcnt(15)
	s_nop 0
	v_lshlrev_b32_e32 v66, 16, v74
	v_and_b32_e32 v67, 0xffff0000, v74
	v_lshlrev_b32_e32 v68, 16, v75
	v_and_b32_e32 v69, 0xffff0000, v75
	v_pk_mul_f32 v[66:67], v[0:1], v[66:67] op_sel_hi:[0,1]
	v_pk_mul_f32 v[68:69], v[0:1], v[68:69] op_sel_hi:[0,1]
	v_ffbh_u32_e32 v0, v65
	v_pk_mul_f32 v[66:67], v[2:3], v[66:67]
	v_pk_mul_f32 v[68:69], v[4:5], v[68:69]
	v_min_u32_e32 v0, 32, v0
	global_store_dwordx4 v[62:63], v[66:69], off offset:3072 sc1
	v_lshlrev_b64 v[62:63], v0, v[64:65]
	v_min_u32_e32 v62, 1, v62
	v_or_b32_e32 v62, v63, v62
	v_cvt_f32_u32_e32 v62, v62
	v_sub_u32_e32 v0, 32, v0
	s_waitcnt vmcnt(15)
	v_and_b32_e32 v63, 0xffff0000, v60
	v_lshl_add_u64 v[66:67], v[34:35], 0, s[0:1]
	v_ldexp_f32 v0, v62, v0
	v_fmamk_f32 v0, v0, 0x32800000, v196
	v_cmp_gt_f32_e32 vcc, s96, v0
	v_mul_f32_e32 v62, 0x4b800000, v0
	v_lshl_add_u64 v[34:35], v[34:35], 0, s[40:41]
	v_cndmask_b32_e32 v0, v0, v62, vcc
	v_rsq_f32_e32 v0, v0
	s_nop 0
	v_mul_f32_e32 v62, 0x45800000, v0
	v_cndmask_b32_e32 v0, v0, v62, vcc
	v_lshlrev_b32_e32 v62, 16, v60
	v_lshlrev_b32_e32 v60, 16, v61
	v_and_b32_e32 v61, 0xffff0000, v61
	v_pk_mul_f32 v[60:61], v[0:1], v[60:61] op_sel_hi:[0,1]
	v_pk_mul_f32 v[62:63], v[0:1], v[62:63] op_sel_hi:[0,1]
	v_pk_mul_f32 v[64:65], v[16:17], v[60:61]
	s_waitcnt vmcnt(14)
	v_lshlrev_b32_e32 v60, 16, v58
	v_and_b32_e32 v61, 0xffff0000, v58
	v_lshlrev_b32_e32 v58, 16, v59
	v_and_b32_e32 v59, 0xffff0000, v59
	v_pk_mul_f32 v[62:63], v[14:15], v[62:63]
	v_pk_mul_f32 v[58:59], v[0:1], v[58:59] op_sel_hi:[0,1]
	global_store_dwordx4 v[66:67], v[62:65], off sc1
	v_pk_mul_f32 v[60:61], v[0:1], v[60:61] op_sel_hi:[0,1]
	v_pk_mul_f32 v[60:61], v[10:11], v[60:61]
	v_pk_mul_f32 v[62:63], v[12:13], v[58:59]
	s_waitcnt vmcnt(14)
	v_lshlrev_b32_e32 v58, 16, v56
	v_and_b32_e32 v59, 0xffff0000, v56
	v_lshlrev_b32_e32 v56, 16, v57
	v_and_b32_e32 v57, 0xffff0000, v57
	v_pk_mul_f32 v[56:57], v[0:1], v[56:57] op_sel_hi:[0,1]
	global_store_dwordx4 v[66:67], v[60:63], off offset:1024 sc1
	v_pk_mul_f32 v[58:59], v[0:1], v[58:59] op_sel_hi:[0,1]
	v_pk_mul_f32 v[58:59], v[6:7], v[58:59]
	v_pk_mul_f32 v[60:61], v[8:9], v[56:57]
	s_waitcnt vmcnt(14)
	v_lshlrev_b32_e32 v56, 16, v54
	v_and_b32_e32 v57, 0xffff0000, v54
	v_lshlrev_b32_e32 v54, 16, v55
	v_and_b32_e32 v55, 0xffff0000, v55
	v_pk_mul_f32 v[56:57], v[0:1], v[56:57] op_sel_hi:[0,1]
	v_pk_mul_f32 v[54:55], v[0:1], v[54:55] op_sel_hi:[0,1]
	v_ffbh_u32_e32 v0, v19
	v_min_u32_e32 v0, 32, v0
	v_lshlrev_b64 v[18:19], v0, v[18:19]
	v_min_u32_e32 v18, 1, v18
	v_or_b32_e32 v18, v19, v18
	v_cvt_f32_u32_e32 v18, v18
	v_sub_u32_e32 v0, 32, v0
	global_store_dwordx4 v[66:67], v[58:61], off offset:2048 sc1
	v_pk_mul_f32 v[56:57], v[2:3], v[56:57]
	v_ldexp_f32 v0, v18, v0
	v_fmamk_f32 v0, v0, 0x32800000, v196
	v_cmp_gt_f32_e32 vcc, s96, v0
	v_mul_f32_e32 v18, 0x4b800000, v0
	v_pk_mul_f32 v[58:59], v[4:5], v[54:55]
	v_cndmask_b32_e32 v0, v0, v18, vcc
	v_rsq_f32_e32 v0, v0
	s_waitcnt vmcnt(14)
	v_lshlrev_b32_e32 v54, 16, v52
	v_and_b32_e32 v55, 0xffff0000, v52
	v_lshlrev_b32_e32 v52, 16, v53
	v_mul_f32_e32 v18, 0x45800000, v0
	v_cndmask_b32_e32 v0, v0, v18, vcc
	v_and_b32_e32 v53, 0xffff0000, v53
	v_pk_mul_f32 v[52:53], v[0:1], v[52:53] op_sel_hi:[0,1]
	global_store_dwordx4 v[66:67], v[56:59], off offset:3072 sc1
	v_pk_mul_f32 v[54:55], v[0:1], v[54:55] op_sel_hi:[0,1]
	v_lshl_add_u64 v[18:19], v[28:29], 0, s[0:1]
	v_pk_mul_f32 v[56:57], v[16:17], v[52:53]
	s_waitcnt vmcnt(14)
	v_lshlrev_b32_e32 v52, 16, v50
	v_and_b32_e32 v53, 0xffff0000, v50
	v_lshlrev_b32_e32 v50, 16, v51
	v_and_b32_e32 v51, 0xffff0000, v51
	v_pk_mul_f32 v[54:55], v[14:15], v[54:55]
	v_pk_mul_f32 v[50:51], v[0:1], v[50:51] op_sel_hi:[0,1]
	global_store_dwordx4 v[18:19], v[54:57], off sc1
	v_pk_mul_f32 v[52:53], v[0:1], v[52:53] op_sel_hi:[0,1]
	v_pk_mul_f32 v[52:53], v[10:11], v[52:53]
	v_pk_mul_f32 v[54:55], v[12:13], v[50:51]
	s_waitcnt vmcnt(14)
	v_lshlrev_b32_e32 v50, 16, v48
	v_and_b32_e32 v51, 0xffff0000, v48
	v_lshlrev_b32_e32 v48, 16, v49
	v_and_b32_e32 v49, 0xffff0000, v49
	v_pk_mul_f32 v[48:49], v[0:1], v[48:49] op_sel_hi:[0,1]
	global_store_dwordx4 v[18:19], v[52:55], off offset:1024 sc1
	v_pk_mul_f32 v[50:51], v[0:1], v[50:51] op_sel_hi:[0,1]
	v_pk_mul_f32 v[50:51], v[6:7], v[50:51]
	v_pk_mul_f32 v[52:53], v[8:9], v[48:49]
	s_waitcnt vmcnt(14)
	v_lshlrev_b32_e32 v48, 16, v46
	v_and_b32_e32 v49, 0xffff0000, v46
	v_lshlrev_b32_e32 v46, 16, v47
	v_and_b32_e32 v47, 0xffff0000, v47
	v_pk_mul_f32 v[48:49], v[0:1], v[48:49] op_sel_hi:[0,1]
	v_pk_mul_f32 v[46:47], v[0:1], v[46:47] op_sel_hi:[0,1]
	v_ffbh_u32_e32 v0, v21
	global_store_dwordx4 v[18:19], v[50:53], off offset:2048 sc1
	v_pk_mul_f32 v[48:49], v[2:3], v[48:49]
	v_min_u32_e32 v0, 32, v0
	v_pk_mul_f32 v[50:51], v[4:5], v[46:47]
	global_store_dwordx4 v[18:19], v[48:51], off offset:3072 sc1
	v_lshlrev_b64 v[18:19], v0, v[20:21]
	v_min_u32_e32 v18, 1, v18
	v_or_b32_e32 v18, v19, v18
	v_cvt_f32_u32_e32 v18, v18
	v_sub_u32_e32 v0, 32, v0
	s_waitcnt vmcnt(15)
	v_and_b32_e32 v19, 0xffff0000, v44
	v_lshlrev_b32_e32 v20, 16, v45
	v_ldexp_f32 v0, v18, v0
	v_fmamk_f32 v0, v0, 0x32800000, v196
	v_cmp_gt_f32_e32 vcc, s96, v0
	v_mul_f32_e32 v18, 0x4b800000, v0
	v_and_b32_e32 v21, 0xffff0000, v45
	v_cndmask_b32_e32 v0, v0, v18, vcc
	v_rsq_f32_e32 v0, v0
	v_lshl_add_u64 v[46:47], v[24:25], 0, s[16:17]
	v_lshl_add_u64 v[28:29], v[28:29], 0, s[40:41]
	v_mul_f32_e32 v18, 0x45800000, v0
	v_cndmask_b32_e32 v0, v0, v18, vcc
	v_lshlrev_b32_e32 v18, 16, v44
	v_pk_mul_f32 v[18:19], v[0:1], v[18:19] op_sel_hi:[0,1]
	v_pk_mul_f32 v[20:21], v[0:1], v[20:21] op_sel_hi:[0,1]
	v_pk_mul_f32 v[18:19], v[14:15], v[18:19]
	v_pk_mul_f32 v[20:21], v[16:17], v[20:21]
	global_store_dwordx4 v[46:47], v[18:21], off sc1
	s_waitcnt vmcnt(15)
	s_nop 0
	v_lshlrev_b32_e32 v18, 16, v42
	v_and_b32_e32 v19, 0xffff0000, v42
	v_lshlrev_b32_e32 v20, 16, v43
	v_and_b32_e32 v21, 0xffff0000, v43
	v_pk_mul_f32 v[18:19], v[0:1], v[18:19] op_sel_hi:[0,1]
	v_pk_mul_f32 v[20:21], v[0:1], v[20:21] op_sel_hi:[0,1]
	v_pk_mul_f32 v[18:19], v[10:11], v[18:19]
	v_pk_mul_f32 v[20:21], v[12:13], v[20:21]
	global_store_dwordx4 v[46:47], v[18:21], off offset:1024 sc1
	s_waitcnt vmcnt(15)
	s_nop 0
	v_lshlrev_b32_e32 v18, 16, v40
	v_and_b32_e32 v19, 0xffff0000, v40
	v_lshlrev_b32_e32 v20, 16, v41
	v_and_b32_e32 v21, 0xffff0000, v41
	v_pk_mul_f32 v[18:19], v[0:1], v[18:19] op_sel_hi:[0,1]
	v_pk_mul_f32 v[20:21], v[0:1], v[20:21] op_sel_hi:[0,1]
	v_pk_mul_f32 v[18:19], v[6:7], v[18:19]
	v_pk_mul_f32 v[20:21], v[8:9], v[20:21]
	global_store_dwordx4 v[46:47], v[18:21], off offset:2048 sc1
	s_waitcnt vmcnt(15)
	s_nop 0
	v_lshlrev_b32_e32 v18, 16, v38
	v_and_b32_e32 v19, 0xffff0000, v38
	v_lshlrev_b32_e32 v20, 16, v39
	v_and_b32_e32 v21, 0xffff0000, v39
	v_pk_mul_f32 v[18:19], v[0:1], v[18:19] op_sel_hi:[0,1]
	v_pk_mul_f32 v[20:21], v[0:1], v[20:21] op_sel_hi:[0,1]
	v_pk_mul_f32 v[18:19], v[2:3], v[18:19]
	v_pk_mul_f32 v[20:21], v[4:5], v[20:21]
	global_store_dwordx4 v[46:47], v[18:21], off offset:3072 sc1
	s_cbranch_scc0 .LBB0_27

.LBB0_43:
	v_add_u32_e32 v79, 0x600, v80
	v_mul_hi_i32 v0, v79, s89
	v_lshrrev_b32_e32 v2, 31, v0
	v_ashrrev_i32_e32 v0, 6, v0
	v_add_u32_e32 v0, v0, v2
	v_mad_i32_i24 v2, v0, s90, v80
	v_lshl_add_u32 v74, v2, 3, v197
	v_ashrrev_i32_e32 v2, 1, v0
	v_add_u32_e32 v66, s34, v2
	v_and_b32_e32 v67, 1, v0
	v_and_b32_e32 v0, 0x7f, v66
	v_mov_b64_e32 v[2:3], s[14:15]
	v_cmp_ne_u32_e32 vcc, 0, v0
	v_mad_i64_i32 v[2:3], s[38:39], v66, s3, v[2:3]
	v_ashrrev_i32_e32 v75, 31, v74
	v_mul_u32_u24_e32 v0, 0xb00, v67
	v_lshl_add_u64 v[2:3], v[74:75], 1, v[2:3]
	v_lshlrev_b32_e32 v0, 1, v0
	v_lshl_add_u64 v[14:15], v[2:3], 0, v[0:1]
	global_load_dwordx4 v[54:57], v[14:15], off nt
	v_cmp_eq_u32_e64 s[38:39], 0, v67
	s_mov_b64 s[64:65], -1
	s_mov_b64 s[40:41], 0
	s_and_saveexec_b64 s[42:43], s[38:39]
	s_cbranch_execz .LBB0_66
	s_mov_b64 s[38:39], 0
	s_mov_b64 s[40:41], -1
	s_and_saveexec_b64 s[64:65], vcc
	s_movk_i32 s40, 0xea00
	s_mov_b32 s41, -1
	s_mov_b64 s[38:39], exec
	v_lshl_add_u64 v[2:3], v[2:3], 0, s[40:41]
	s_xor_b64 s[40:41], exec, -1
	s_or_b64 exec, exec, s[64:65]
	s_and_b64 s[40:41], s[40:41], exec
	s_orn2_b64 s[64:65], s[38:39], exec
	s_or_b64 exec, exec, s[42:43]
	s_and_saveexec_b64 s[38:39], s[64:65]
	s_cbranch_execnz .LBB0_67

.LBB0_49:
	s_or_b64 exec, exec, s[38:39]
	v_lshl_or_b32 v16, v66, 1, v67
	v_mov_b64_e32 v[14:15], s[16:17]
	v_ashrrev_i32_e32 v0, 31, v66
	v_mad_u64_u32 v[14:15], s[38:39], v16, s2, v[14:15]
	v_mad_i32_i24 v15, v0, s2, v15
	v_lshl_add_u64 v[14:15], v[74:75], 1, v[14:15]
	global_load_dwordx4 v[50:53], v[14:15], off nt
	v_add_u32_e32 v0, 0x800, v80
	s_movk_i32 s29, 0x900
	v_mul_hi_i32 v0, v0, s89
	s_waitcnt vmcnt(1)
	v_mov_b64_e32 v[24:25], v[12:13]
	v_cmp_gt_i32_e64 s[40:41], s29, v79
	v_lshrrev_b32_e32 v83, 31, v0
	v_ashrrev_i32_e32 v84, 6, v0
	v_mov_b64_e32 v[22:23], v[10:11]
	v_mov_b64_e32 v[20:21], v[8:9]
	v_mov_b64_e32 v[18:19], v[6:7]
	v_mov_b64_e32 v[16:17], v[4:5]
	v_mov_b64_e32 v[14:15], v[2:3]
	s_and_saveexec_b64 s[42:43], s[40:41]
	s_cbranch_execz .LBB0_57
	v_add_u32_e32 v0, v84, v83
	v_mad_i32_i24 v6, v0, s90, v80
	v_lshl_add_u32 v14, v6, 3, v234
	v_ashrrev_i32_e32 v6, 1, v0
	v_add_u32_e32 v18, s34, v6
	v_and_b32_e32 v19, 1, v0
	v_and_b32_e32 v0, 0x7f, v18
	v_mov_b64_e32 v[6:7], s[14:15]
	v_cmp_ne_u32_e32 vcc, 0, v0
	v_mad_i64_i32 v[6:7], s[38:39], v18, s3, v[6:7]
	v_ashrrev_i32_e32 v15, 31, v14
	v_mul_u32_u24_e32 v0, 0xb00, v19
	v_lshl_add_u64 v[6:7], v[14:15], 1, v[6:7]
	v_lshlrev_b32_e32 v0, 1, v0
	v_lshl_add_u64 v[16:17], v[6:7], 0, v[0:1]
	global_load_dwordx4 v[26:29], v[16:17], off nt
	v_cmp_eq_u32_e64 s[38:39], 0, v19
	s_mov_b64 s[82:83], -1
	s_mov_b64 s[64:65], 0
	s_and_saveexec_b64 s[66:67], s[38:39]
	s_cbranch_execz .LBB0_70
	s_mov_b64 s[38:39], 0
	s_mov_b64 s[64:65], -1
	s_and_saveexec_b64 s[82:83], vcc
	s_movk_i32 s46, 0xea00
	s_mov_b32 s47, -1
	s_mov_b64 s[38:39], exec
	v_lshl_add_u64 v[6:7], v[6:7], 0, s[46:47]
	s_xor_b64 s[64:65], exec, -1
	s_or_b64 exec, exec, s[82:83]
	s_and_b64 s[64:65], s[64:65], exec
	s_orn2_b64 s[82:83], s[38:39], exec
	s_or_b64 exec, exec, s[66:67]
	s_and_saveexec_b64 s[38:39], s[82:83]
	s_cbranch_execnz .LBB0_71

.LBB0_56:
	s_or_b64 exec, exec, s[38:39]
	v_ashrrev_i32_e32 v0, 31, v18
	v_lshl_or_b32 v18, v18, 1, v19
	v_mov_b64_e32 v[16:17], s[16:17]
	v_mad_u64_u32 v[16:17], s[38:39], v18, s2, v[16:17]
	v_mad_i32_i24 v17, v0, s2, v17
	v_lshl_add_u64 v[14:15], v[14:15], 1, v[16:17]
	global_load_dwordx4 v[46:49], v[14:15], off nt
	s_waitcnt vmcnt(1)
	v_mov_b64_e32 v[24:25], v[12:13]
	v_mov_b64_e32 v[22:23], v[10:11]
	v_mov_b64_e32 v[20:21], v[8:9]
	v_mov_b64_e32 v[18:19], v[6:7]
	v_mov_b64_e32 v[16:17], v[4:5]
	v_mov_b64_e32 v[14:15], v[2:3]
.LBB0_57:
	s_or_b64 exec, exec, s[42:43]
	v_add_u32_e32 v0, 0xa00, v80
	s_movk_i32 s29, 0x700
	v_mul_hi_i32 v0, v0, s89
	v_cmp_gt_i32_e64 s[38:39], s29, v79
	v_lshrrev_b32_e32 v81, 31, v0
	v_ashrrev_i32_e32 v82, 6, v0
	s_and_saveexec_b64 s[64:65], s[38:39]
	s_cbranch_execz .LBB0_77
	v_add_u32_e32 v0, v82, v81
	v_ashrrev_i32_e32 v11, 1, v0
	v_mad_i32_i24 v10, v0, s90, v80
	v_add_u32_e32 v12, s34, v11
	v_lshl_add_u32 v10, v10, 3, v230
	v_and_b32_e32 v18, 1, v0
	v_and_b32_e32 v0, 0x7f, v12
	v_mov_b64_e32 v[14:15], s[14:15]
	v_cmp_ne_u32_e32 vcc, 0, v0
	v_mad_i64_i32 v[14:15], s[42:43], v12, s3, v[14:15]
	v_ashrrev_i32_e32 v11, 31, v10
	v_mul_u32_u24_e32 v0, 0xb00, v18
	v_lshl_add_u64 v[16:17], v[10:11], 1, v[14:15]
	v_lshlrev_b32_e32 v0, 1, v0
	v_lshl_add_u64 v[14:15], v[16:17], 0, v[0:1]
	global_load_dwordx4 v[30:33], v[14:15], off nt
	v_cmp_eq_u32_e64 s[42:43], 0, v18
	s_mov_b64 s[84:85], -1
	s_mov_b64 s[66:67], 0
	s_and_saveexec_b64 s[82:83], s[42:43]
	s_cbranch_execz .LBB0_62
	s_mov_b64 s[42:43], 0
	s_mov_b64 s[66:67], -1
	s_and_saveexec_b64 s[84:85], vcc
	s_movk_i32 s46, 0xea00
	s_mov_b32 s47, -1
	s_mov_b64 s[42:43], exec
	v_lshl_add_u64 v[16:17], v[16:17], 0, s[46:47]
	s_xor_b64 s[66:67], exec, -1
	s_or_b64 exec, exec, s[84:85]
	s_and_b64 s[66:67], s[66:67], exec
	s_orn2_b64 s[84:85], s[42:43], exec
.LBB0_62:
	s_or_b64 exec, exec, s[82:83]
	s_and_saveexec_b64 s[42:43], s[84:85]
	s_cbranch_execz .LBB0_74
	global_load_dwordx4 v[62:65], v[16:17], off nt
	v_mov_b32_e32 v37, 0
	v_mov_b32_e32 v36, 0
	v_mov_b32_e32 v35, 0
	v_mov_b32_e32 v34, 0
	s_and_saveexec_b64 s[82:83], vcc
	s_cbranch_execz .LBB0_65
	v_add_co_u32_e32 v14, vcc, 0xffffe000, v14
	s_nop 1
	v_addc_co_u32_e32 v15, vcc, -1, v15, vcc
	global_load_dwordx4 v[34:37], v[14:15], off offset:-3072 nt

.LBB0_67:
	global_load_dwordx4 v[2:5], v[2:3], off nt
	v_mov_b32_e32 v61, 0
	v_mov_b32_e32 v60, 0
	v_mov_b32_e32 v59, 0
	v_mov_b32_e32 v58, 0
	s_and_saveexec_b64 s[42:43], vcc
	s_cbranch_execz .LBB0_69
	v_add_co_u32_e32 v14, vcc, 0xffffe000, v14
	s_nop 1
	v_addc_co_u32_e32 v15, vcc, -1, v15, vcc
	global_load_dwordx4 v[58:61], v[14:15], off offset:-3072 nt

.LBB0_71:
	global_load_dwordx4 v[6:9], v[6:7], off nt
	v_mov_b32_e32 v41, 0
	v_mov_b32_e32 v40, 0
	v_mov_b32_e32 v39, 0
	v_mov_b32_e32 v38, 0
	s_and_saveexec_b64 s[66:67], vcc
	s_cbranch_execz .LBB0_73
	v_add_co_u32_e32 v16, vcc, 0xffffe000, v16
	s_nop 1
	v_addc_co_u32_e32 v17, vcc, -1, v17, vcc
	global_load_dwordx4 v[38:41], v[16:17], off offset:-3072 nt

.LBB0_76:
	s_or_b64 exec, exec, s[42:43]
	v_ashrrev_i32_e32 v0, 31, v12
	v_lshl_or_b32 v12, v12, 1, v18
	v_mov_b64_e32 v[14:15], s[16:17]
	v_mad_u64_u32 v[14:15], s[42:43], v12, s2, v[14:15]
	v_mad_i32_i24 v15, v0, s2, v15
	v_lshl_add_u64 v[10:11], v[10:11], 1, v[14:15]
	global_load_dwordx4 v[42:45], v[10:11], off nt
	s_waitcnt vmcnt(1)
	v_mov_b32_e32 v12, v64
	v_mov_b32_e32 v10, v62
	v_mov_b32_e32 v11, v63
	v_mov_b64_e32 v[24:25], v[12:13]
	v_mov_b64_e32 v[22:23], v[10:11]
	v_mov_b64_e32 v[20:21], v[8:9]
	v_mov_b64_e32 v[18:19], v[6:7]
	v_mov_b64_e32 v[16:17], v[4:5]
	v_mov_b64_e32 v[14:15], v[2:3]
	v_mov_b32_e32 v25, v65
	v_mov_b32_e32 v13, v65
.LBB0_77:
	s_or_b64 exec, exec, s[64:65]
	v_lshlrev_b64 v[70:71], 2, v[74:75]
	v_lshl_add_u64 v[2:3], s[56:57], 0, v[70:71]
	v_lshl_or_b32 v0, v66, 6, v67
	global_load_dwordx4 v[66:69], v[2:3], off offset:16 nt
	global_load_dwordx4 v[86:89], v[2:3], off nt
	v_lshl_add_u64 v[2:3], s[60:61], 0, v[70:71]
	v_lshl_add_u64 v[72:73], s[62:63], 0, v[70:71]
	v_lshl_add_u64 v[76:77], s[58:59], 0, v[70:71]
	global_load_dwordx4 v[62:65], v[2:3], off offset:16 nt
	global_load_dwordx4 v[90:93], v[2:3], off nt
	s_nop 0
	global_load_dwordx4 v[2:5], v[72:73], off offset:16 nt
	global_load_dwordx4 v[94:97], v[72:73], off nt
	s_nop 0
	global_load_dwordx4 v[70:73], v[76:77], off offset:16 nt
	global_load_dwordx4 v[98:101], v[76:77], off nt
	v_lshlrev_b32_e32 v76, 16, v58
	v_and_b32_e32 v77, 0xffff0000, v58
	v_lshlrev_b32_e32 v58, 16, v59
	v_and_b32_e32 v59, 0xffff0000, v59
	s_waitcnt vmcnt(0)
	v_pk_fma_f32 v[76:77], v[86:87], v[76:77], v[98:99]
	v_lshlrev_b32_e32 v86, 16, v14
	v_and_b32_e32 v87, 0xffff0000, v14
	v_pk_fma_f32 v[76:77], v[90:91], v[86:87], v[76:77]
	v_lshlrev_b32_e32 v86, 16, v54
	v_and_b32_e32 v87, 0xffff0000, v54
	v_pk_fma_f32 v[76:77], v[94:95], v[86:87], v[76:77]
	v_pk_fma_f32 v[58:59], v[88:89], v[58:59], v[100:101]
	v_mul_f32_e32 v14, 0x3d372713, v76
	v_mul_f32_e32 v14, v76, v14
	v_fma_f32 v14, v76, v14, v76
	v_mul_f32_e32 v14, 0xc0135761, v14
	v_exp_f32_e32 v14, v14
	v_lshlrev_b32_e32 v54, 16, v55
	v_and_b32_e32 v55, 0xffff0000, v55
	v_add_f32_e32 v14, 1.0, v14
	v_rcp_f32_e32 v86, v14
	v_mul_f32_e32 v14, 0x3d372713, v77
	v_mul_f32_e32 v14, v77, v14
	v_fma_f32 v14, v77, v14, v77
	v_mul_f32_e32 v14, 0xc0135761, v14
	v_exp_f32_e32 v14, v14
	s_nop 0
	v_add_f32_e32 v14, 1.0, v14
	v_rcp_f32_e32 v87, v14
	v_lshlrev_b32_e32 v14, 16, v15
	v_and_b32_e32 v15, 0xffff0000, v15
	v_pk_fma_f32 v[14:15], v[92:93], v[14:15], v[58:59]
	v_pk_mul_f32 v[76:77], v[76:77], v[86:87]
	v_pk_fma_f32 v[14:15], v[96:97], v[54:55], v[14:15]
	v_lshlrev_b32_e32 v86, 16, v50
	v_and_b32_e32 v87, 0xffff0000, v50
	v_mul_f32_e32 v50, 0x3d372713, v14
	v_mul_f32_e32 v50, v14, v50
	v_fma_f32 v50, v14, v50, v14
	v_mul_f32_e32 v50, 0xc0135761, v50
	v_exp_f32_e32 v50, v50
	v_pk_mul_f32 v[76:77], v[76:77], v[86:87]
	v_add_f32_e32 v50, 1.0, v50
	v_rcp_f32_e32 v54, v50
	v_mul_f32_e32 v50, 0x3d372713, v15
	v_mul_f32_e32 v50, v15, v50
	v_fma_f32 v50, v15, v50, v15
	v_mul_f32_e32 v50, 0xc0135761, v50
	v_exp_f32_e32 v50, v50
	s_nop 0
	v_add_f32_e32 v50, 1.0, v50
	v_rcp_f32_e32 v55, v50
	v_lshlrev_b32_e32 v50, 16, v51
	v_and_b32_e32 v51, 0xffff0000, v51
	v_pk_mul_f32 v[14:15], v[14:15], v[54:55]
	s_nop 0
	v_pk_mul_f32 v[14:15], v[14:15], v[50:51]
	v_lshlrev_b32_e32 v50, 16, v60
	v_and_b32_e32 v51, 0xffff0000, v60
	v_pk_fma_f32 v[50:51], v[66:67], v[50:51], v[70:71]
	v_lshlrev_b32_e32 v54, 16, v16
	v_and_b32_e32 v55, 0xffff0000, v16
	v_pk_fma_f32 v[50:51], v[62:63], v[54:55], v[50:51]
	v_lshlrev_b32_e32 v54, 16, v56
	v_and_b32_e32 v55, 0xffff0000, v56
	v_pk_fma_f32 v[2:3], v[2:3], v[54:55], v[50:51]
	s_nop 0
	v_mul_f32_e32 v16, 0x3d372713, v2
	v_mul_f32_e32 v16, v2, v16
	v_fma_f32 v16, v2, v16, v2
	v_mul_f32_e32 v16, 0xc0135761, v16
	v_exp_f32_e32 v16, v16
	s_nop 0
	v_add_f32_e32 v16, 1.0, v16
	v_rcp_f32_e32 v50, v16
	v_mul_f32_e32 v16, 0x3d372713, v3
	v_mul_f32_e32 v16, v3, v16
	v_fma_f32 v16, v3, v16, v3
	v_mul_f32_e32 v16, 0xc0135761, v16
	v_exp_f32_e32 v16, v16
	s_nop 0
	v_add_f32_e32 v16, 1.0, v16
	v_rcp_f32_e32 v51, v16
	v_lshlrev_b32_e32 v16, 16, v17
	v_and_b32_e32 v17, 0xffff0000, v17
	v_pk_mul_f32 v[2:3], v[2:3], v[50:51]
	v_lshlrev_b32_e32 v50, 16, v52
	v_and_b32_e32 v51, 0xffff0000, v52
	v_pk_mul_f32 v[2:3], v[2:3], v[50:51]
	v_lshlrev_b32_e32 v50, 16, v61
	v_and_b32_e32 v51, 0xffff0000, v61
	v_pk_fma_f32 v[50:51], v[68:69], v[50:51], v[72:73]
	v_cvt_pk_bf16_f32 v52, v2, v3
	v_pk_fma_f32 v[16:17], v[64:65], v[16:17], v[50:51]
	v_lshlrev_b32_e32 v50, 16, v57
	v_and_b32_e32 v51, 0xffff0000, v57
	v_pk_fma_f32 v[4:5], v[4:5], v[50:51], v[16:17]
	v_mov_b64_e32 v[2:3], s[0:1]
	v_mul_f32_e32 v16, 0x3d372713, v4
	v_mul_f32_e32 v17, 0x3d372713, v5
	v_mul_f32_e32 v16, v4, v16
	v_mul_f32_e32 v17, v5, v17
	v_fma_f32 v16, v4, v16, v4
	v_fma_f32 v17, v5, v17, v5
	v_mul_f32_e32 v16, 0xc0135761, v16
	v_mul_f32_e32 v17, 0xc0135761, v17
	v_exp_f32_e32 v16, v16
	v_exp_f32_e32 v17, v17
	v_mad_i64_i32 v[2:3], s[42:43], v0, s2, v[2:3]
	v_add_f32_e32 v16, 1.0, v16
	v_add_f32_e32 v17, 1.0, v17
	v_rcp_f32_e32 v16, v16
	v_rcp_f32_e32 v17, v17
	v_cvt_pk_bf16_f32 v50, v76, v77
	v_cvt_pk_bf16_f32 v51, v14, v15
	v_lshl_add_u64 v[2:3], v[74:75], 1, v[2:3]
	v_pk_mul_f32 v[4:5], v[4:5], v[16:17]
	v_lshlrev_b32_e32 v16, 16, v53
	v_and_b32_e32 v17, 0xffff0000, v53
	v_pk_mul_f32 v[4:5], v[4:5], v[16:17]
	s_nop 0
	v_cvt_pk_bf16_f32 v53, v4, v5
	global_store_dwordx4 v[2:3], v[50:53], off sc1
	s_and_saveexec_b64 s[42:43], s[40:41]
	s_cbranch_execz .LBB0_79
	v_add_u32_e32 v0, v84, v83
	v_mad_i32_i24 v2, v0, s90, v80
	v_lshl_add_u32 v58, v2, 3, v234
	v_lshrrev_b32_e32 v2, 1, v0
	v_ashrrev_i32_e32 v59, 31, v58
	v_add_u32_e32 v2, s34, v2
	v_and_b32_e32 v0, 1, v0
	v_lshlrev_b64 v[54:55], 2, v[58:59]
	v_lshl_or_b32 v0, v2, 6, v0
	v_lshl_add_u64 v[2:3], s[56:57], 0, v[54:55]
	global_load_dwordx4 v[50:53], v[2:3], off offset:16 nt
	global_load_dwordx4 v[60:63], v[2:3], off nt
	v_lshl_add_u64 v[2:3], s[60:61], 0, v[54:55]
	v_lshl_add_u64 v[56:57], s[62:63], 0, v[54:55]
	v_lshl_add_u64 v[72:73], s[58:59], 0, v[54:55]
	global_load_dwordx4 v[14:17], v[2:3], off offset:16 nt
	global_load_dwordx4 v[64:67], v[2:3], off nt
	s_nop 0
	global_load_dwordx4 v[2:5], v[56:57], off offset:16 nt
	global_load_dwordx4 v[68:71], v[56:57], off nt
	s_nop 0
	global_load_dwordx4 v[54:57], v[72:73], off offset:16 nt
	s_nop 0
	global_load_dwordx4 v[72:75], v[72:73], off nt
	v_lshlrev_b32_e32 v76, 16, v38
	v_and_b32_e32 v77, 0xffff0000, v38
	s_waitcnt vmcnt(0)
	v_pk_fma_f32 v[60:61], v[60:61], v[76:77], v[72:73]
	v_lshlrev_b32_e32 v72, 16, v18
	v_and_b32_e32 v73, 0xffff0000, v18
	v_pk_fma_f32 v[60:61], v[64:65], v[72:73], v[60:61]
	v_lshlrev_b32_e32 v64, 16, v26
	v_and_b32_e32 v65, 0xffff0000, v26
	v_pk_fma_f32 v[60:61], v[68:69], v[64:65], v[60:61]
	s_nop 0
	v_mul_f32_e32 v18, 0x3d372713, v60
	v_mul_f32_e32 v18, v60, v18
	v_fma_f32 v18, v60, v18, v60
	v_mul_f32_e32 v18, 0xc0135761, v18
	v_exp_f32_e32 v18, v18
	s_nop 0
	v_add_f32_e32 v18, 1.0, v18
	v_rcp_f32_e32 v64, v18
	v_mul_f32_e32 v18, 0x3d372713, v61
	v_mul_f32_e32 v18, v61, v18
	v_fma_f32 v18, v61, v18, v61
	v_mul_f32_e32 v18, 0xc0135761, v18
	v_exp_f32_e32 v18, v18
	s_nop 0
	v_add_f32_e32 v18, 1.0, v18
	v_rcp_f32_e32 v65, v18
	v_lshlrev_b32_e32 v18, 16, v19
	v_and_b32_e32 v19, 0xffff0000, v19
	v_pk_mul_f32 v[60:61], v[60:61], v[64:65]
	v_lshlrev_b32_e32 v64, 16, v46
	v_and_b32_e32 v65, 0xffff0000, v46
	v_pk_mul_f32 v[60:61], v[60:61], v[64:65]
	v_lshlrev_b32_e32 v64, 16, v39
	v_and_b32_e32 v65, 0xffff0000, v39
	v_pk_fma_f32 v[62:63], v[62:63], v[64:65], v[74:75]
	s_nop 0
	v_pk_fma_f32 v[18:19], v[66:67], v[18:19], v[62:63]
	v_lshlrev_b32_e32 v62, 16, v27
	v_and_b32_e32 v63, 0xffff0000, v27
	v_pk_fma_f32 v[18:19], v[70:71], v[62:63], v[18:19]
	s_nop 0
	v_mul_f32_e32 v62, 0x3d372713, v18
	v_mul_f32_e32 v63, 0x3d372713, v19
	v_mul_f32_e32 v62, v18, v62
	v_mul_f32_e32 v63, v19, v63
	v_fma_f32 v62, v18, v62, v18
	v_fma_f32 v63, v19, v63, v19
	v_mul_f32_e32 v62, 0xc0135761, v62
	v_mul_f32_e32 v63, 0xc0135761, v63
	v_exp_f32_e32 v62, v62
	v_exp_f32_e32 v63, v63
	v_add_f32_e32 v62, 1.0, v62
	v_add_f32_e32 v63, 1.0, v63
	v_rcp_f32_e32 v62, v62
	v_rcp_f32_e32 v63, v63
	s_nop 0
	v_pk_mul_f32 v[18:19], v[18:19], v[62:63]
	v_lshlrev_b32_e32 v62, 16, v47
	v_and_b32_e32 v63, 0xffff0000, v47
	v_pk_mul_f32 v[18:19], v[18:19], v[62:63]
	v_lshlrev_b32_e32 v62, 16, v40
	v_and_b32_e32 v63, 0xffff0000, v40
	v_pk_fma_f32 v[50:51], v[50:51], v[62:63], v[54:55]
	v_lshlrev_b32_e32 v54, 16, v20
	v_and_b32_e32 v55, 0xffff0000, v20
	v_pk_fma_f32 v[14:15], v[14:15], v[54:55], v[50:51]
	v_lshlrev_b32_e32 v50, 16, v28
	v_and_b32_e32 v51, 0xffff0000, v28
	v_pk_fma_f32 v[2:3], v[2:3], v[50:51], v[14:15]
	v_lshlrev_b32_e32 v20, 16, v21
	v_mul_f32_e32 v14, 0x3d372713, v2
	v_mul_f32_e32 v15, 0x3d372713, v3
	v_mul_f32_e32 v14, v2, v14
	v_mul_f32_e32 v15, v3, v15
	v_fma_f32 v14, v2, v14, v2
	v_fma_f32 v15, v3, v15, v3
	v_mul_f32_e32 v14, 0xc0135761, v14
	v_mul_f32_e32 v15, 0xc0135761, v15
	v_exp_f32_e32 v14, v14
	v_exp_f32_e32 v15, v15
	v_and_b32_e32 v21, 0xffff0000, v21
	v_add_f32_e32 v14, 1.0, v14
	v_add_f32_e32 v15, 1.0, v15
	v_rcp_f32_e32 v14, v14
	v_rcp_f32_e32 v15, v15
	s_nop 0
	v_pk_mul_f32 v[2:3], v[2:3], v[14:15]
	v_lshlrev_b32_e32 v14, 16, v48
	v_and_b32_e32 v15, 0xffff0000, v48
	v_pk_mul_f32 v[2:3], v[2:3], v[14:15]
	v_lshlrev_b32_e32 v14, 16, v41
	v_and_b32_e32 v15, 0xffff0000, v41
	v_pk_fma_f32 v[14:15], v[52:53], v[14:15], v[56:57]
	s_nop 0
	v_pk_fma_f32 v[14:15], v[16:17], v[20:21], v[14:15]
	v_lshlrev_b32_e32 v16, 16, v29
	v_and_b32_e32 v17, 0xffff0000, v29
	v_pk_fma_f32 v[4:5], v[4:5], v[16:17], v[14:15]
	v_cvt_pk_bf16_f32 v16, v2, v3
	v_mul_f32_e32 v14, 0x3d372713, v4
	v_mul_f32_e32 v15, 0x3d372713, v5
	v_mul_f32_e32 v14, v4, v14
	v_mul_f32_e32 v15, v5, v15
	v_fma_f32 v14, v4, v14, v4
	v_fma_f32 v15, v5, v15, v5
	v_mul_f32_e32 v14, 0xc0135761, v14
	v_mul_f32_e32 v15, 0xc0135761, v15
	v_exp_f32_e32 v14, v14
	v_exp_f32_e32 v15, v15
	v_mov_b64_e32 v[2:3], s[0:1]
	v_mad_i64_i32 v[2:3], s[40:41], v0, s2, v[2:3]
	v_add_f32_e32 v14, 1.0, v14
	v_add_f32_e32 v15, 1.0, v15
	v_rcp_f32_e32 v14, v14
	v_rcp_f32_e32 v15, v15
	v_lshl_add_u64 v[2:3], v[58:59], 1, v[2:3]
	v_pk_mul_f32 v[4:5], v[4:5], v[14:15]
	v_lshlrev_b32_e32 v14, 16, v49
	v_and_b32_e32 v15, 0xffff0000, v49
	v_pk_mul_f32 v[4:5], v[4:5], v[14:15]
	v_cvt_pk_bf16_f32 v14, v60, v61
	v_cvt_pk_bf16_f32 v15, v18, v19
	v_cvt_pk_bf16_f32 v17, v4, v5
	global_store_dwordx4 v[2:3], v[14:17], off sc1
.LBB0_79:
	s_or_b64 exec, exec, s[42:43]
	s_and_saveexec_b64 s[40:41], s[38:39]
	s_cbranch_execz .LBB0_42
	v_add_u32_e32 v0, v82, v81
	v_mad_i32_i24 v2, v0, s90, v80
	v_lshl_add_u32 v54, v2, 3, v230
	v_lshrrev_b32_e32 v2, 1, v0
	v_ashrrev_i32_e32 v55, 31, v54
	v_add_u32_e32 v2, s34, v2
	v_and_b32_e32 v0, 1, v0
	v_lshlrev_b64 v[50:51], 2, v[54:55]
	v_lshl_or_b32 v0, v2, 6, v0
	v_lshl_add_u64 v[2:3], s[56:57], 0, v[50:51]
	global_load_dwordx4 v[18:21], v[2:3], off offset:16 nt
	global_load_dwordx4 v[56:59], v[2:3], off nt
	v_lshl_add_u64 v[2:3], s[60:61], 0, v[50:51]
	v_lshl_add_u64 v[52:53], s[62:63], 0, v[50:51]
	v_lshl_add_u64 v[68:69], s[58:59], 0, v[50:51]
	global_load_dwordx4 v[14:17], v[2:3], off offset:16 nt
	global_load_dwordx4 v[60:63], v[2:3], off nt
	s_nop 0
	global_load_dwordx4 v[2:5], v[52:53], off offset:16 nt
	global_load_dwordx4 v[64:67], v[52:53], off nt
	s_nop 0
	global_load_dwordx4 v[50:53], v[68:69], off offset:16 nt
	s_nop 0
	global_load_dwordx4 v[68:71], v[68:69], off nt
	v_lshlrev_b32_e32 v72, 16, v34
	v_and_b32_e32 v73, 0xffff0000, v34
	s_waitcnt vmcnt(0)
	v_pk_fma_f32 v[56:57], v[56:57], v[72:73], v[68:69]
	v_lshlrev_b32_e32 v68, 16, v22
	v_and_b32_e32 v69, 0xffff0000, v22
	v_pk_fma_f32 v[56:57], v[60:61], v[68:69], v[56:57]
	v_lshlrev_b32_e32 v60, 16, v30
	v_and_b32_e32 v61, 0xffff0000, v30
	v_pk_fma_f32 v[56:57], v[64:65], v[60:61], v[56:57]
	s_nop 0
	v_mul_f32_e32 v22, 0x3d372713, v56
	v_mul_f32_e32 v22, v56, v22
	v_fma_f32 v22, v56, v22, v56
	v_mul_f32_e32 v22, 0xc0135761, v22
	v_exp_f32_e32 v22, v22
	s_nop 0
	v_add_f32_e32 v22, 1.0, v22
	v_rcp_f32_e32 v60, v22
	v_mul_f32_e32 v22, 0x3d372713, v57
	v_mul_f32_e32 v22, v57, v22
	v_fma_f32 v22, v57, v22, v57
	v_mul_f32_e32 v22, 0xc0135761, v22
	v_exp_f32_e32 v22, v22
	s_nop 0
	v_add_f32_e32 v22, 1.0, v22
	v_rcp_f32_e32 v61, v22
	v_lshlrev_b32_e32 v22, 16, v23
	v_and_b32_e32 v23, 0xffff0000, v23
	v_pk_mul_f32 v[56:57], v[56:57], v[60:61]
	v_lshlrev_b32_e32 v60, 16, v42
	v_and_b32_e32 v61, 0xffff0000, v42
	v_pk_mul_f32 v[56:57], v[56:57], v[60:61]
	v_lshlrev_b32_e32 v60, 16, v35
	v_and_b32_e32 v61, 0xffff0000, v35
	v_pk_fma_f32 v[58:59], v[58:59], v[60:61], v[70:71]
	s_nop 0
	v_pk_fma_f32 v[22:23], v[62:63], v[22:23], v[58:59]
	v_lshlrev_b32_e32 v58, 16, v31
	v_and_b32_e32 v59, 0xffff0000, v31
	v_pk_fma_f32 v[22:23], v[66:67], v[58:59], v[22:23]
	s_nop 0
	v_mul_f32_e32 v58, 0x3d372713, v22
	v_mul_f32_e32 v59, 0x3d372713, v23
	v_mul_f32_e32 v58, v22, v58
	v_mul_f32_e32 v59, v23, v59
	v_fma_f32 v58, v22, v58, v22
	v_fma_f32 v59, v23, v59, v23
	v_mul_f32_e32 v58, 0xc0135761, v58
	v_mul_f32_e32 v59, 0xc0135761, v59
	v_exp_f32_e32 v58, v58
	v_exp_f32_e32 v59, v59
	v_add_f32_e32 v58, 1.0, v58
	v_add_f32_e32 v59, 1.0, v59
	v_rcp_f32_e32 v58, v58
	v_rcp_f32_e32 v59, v59
	s_nop 0
	v_pk_mul_f32 v[22:23], v[22:23], v[58:59]
	v_lshlrev_b32_e32 v58, 16, v43
	v_and_b32_e32 v59, 0xffff0000, v43
	v_pk_mul_f32 v[22:23], v[22:23], v[58:59]
	v_lshlrev_b32_e32 v58, 16, v36
	v_and_b32_e32 v59, 0xffff0000, v36
	v_pk_fma_f32 v[18:19], v[18:19], v[58:59], v[50:51]
	v_lshlrev_b32_e32 v50, 16, v24
	v_and_b32_e32 v51, 0xffff0000, v24
	v_pk_fma_f32 v[14:15], v[14:15], v[50:51], v[18:19]
	v_lshlrev_b32_e32 v18, 16, v32
	v_and_b32_e32 v19, 0xffff0000, v32
	v_pk_fma_f32 v[2:3], v[2:3], v[18:19], v[14:15]
	v_lshlrev_b32_e32 v18, 16, v25
	v_mul_f32_e32 v14, 0x3d372713, v2
	v_mul_f32_e32 v15, 0x3d372713, v3
	v_mul_f32_e32 v14, v2, v14
	v_mul_f32_e32 v15, v3, v15
	v_fma_f32 v14, v2, v14, v2
	v_fma_f32 v15, v3, v15, v3
	v_mul_f32_e32 v14, 0xc0135761, v14
	v_mul_f32_e32 v15, 0xc0135761, v15
	v_exp_f32_e32 v14, v14
	v_exp_f32_e32 v15, v15
	v_and_b32_e32 v19, 0xffff0000, v25
	v_add_f32_e32 v14, 1.0, v14
	v_add_f32_e32 v15, 1.0, v15
	v_rcp_f32_e32 v14, v14
	v_rcp_f32_e32 v15, v15
	s_nop 0
	v_pk_mul_f32 v[2:3], v[2:3], v[14:15]
	v_lshlrev_b32_e32 v14, 16, v44
	v_and_b32_e32 v15, 0xffff0000, v44
	v_pk_mul_f32 v[2:3], v[2:3], v[14:15]
	v_lshlrev_b32_e32 v14, 16, v37
	v_and_b32_e32 v15, 0xffff0000, v37
	v_pk_fma_f32 v[14:15], v[20:21], v[14:15], v[52:53]
	s_nop 0
	v_pk_fma_f32 v[14:15], v[16:17], v[18:19], v[14:15]
	v_lshlrev_b32_e32 v16, 16, v33
	v_and_b32_e32 v17, 0xffff0000, v33
	v_pk_fma_f32 v[4:5], v[4:5], v[16:17], v[14:15]
	v_cvt_pk_bf16_f32 v16, v2, v3
	v_mul_f32_e32 v14, 0x3d372713, v4
	v_mul_f32_e32 v15, 0x3d372713, v5
	v_mul_f32_e32 v14, v4, v14
	v_mul_f32_e32 v15, v5, v15
	v_fma_f32 v14, v4, v14, v4
	v_fma_f32 v15, v5, v15, v5
	v_mul_f32_e32 v14, 0xc0135761, v14
	v_mul_f32_e32 v15, 0xc0135761, v15
	v_exp_f32_e32 v14, v14
	v_exp_f32_e32 v15, v15
	v_mov_b64_e32 v[2:3], s[0:1]
	v_mad_i64_i32 v[2:3], s[38:39], v0, s2, v[2:3]
	v_add_f32_e32 v14, 1.0, v14
	v_add_f32_e32 v15, 1.0, v15
	v_rcp_f32_e32 v14, v14
	v_rcp_f32_e32 v15, v15
	v_lshl_add_u64 v[2:3], v[54:55], 1, v[2:3]
	v_pk_mul_f32 v[4:5], v[4:5], v[14:15]
	v_lshlrev_b32_e32 v14, 16, v45
	v_and_b32_e32 v15, 0xffff0000, v45
	v_pk_mul_f32 v[4:5], v[4:5], v[14:15]
	v_cvt_pk_bf16_f32 v14, v56, v57
	v_cvt_pk_bf16_f32 v15, v22, v23
	v_cvt_pk_bf16_f32 v17, v4, v5
	global_store_dwordx4 v[2:3], v[14:17], off sc1
	s_branch .LBB0_42

.LBB0_105:
	s_add_u32 s16, s74, 0x2200000
	v_readlane_b32 s0, v253, 39
	s_addc_u32 s17, s75, 0
	v_readlane_b32 s1, v253, 40
	s_and_b64 s[0:1], s[0:1], exec
	v_readlane_b32 s0, v253, 34
	s_cselect_b32 s14, s0, s16
	s_mov_b32 s0, -1
	v_readlane_b32 s1, v253, 35
	s_waitcnt vmcnt(0)
	s_barrier
	s_cselect_b32 s15, s1, s17
	v_mbcnt_lo_u32_b32 v0, s0, 0
	v_mbcnt_hi_u32_b32 v170, s0, v0
	s_ashr_i32 s39, s38, 31
	s_lshl_b32 s1, s62, 5
	s_lshl_b64 s[34:35], s[38:39], 8
	v_lshrrev_b32_e32 v0, 1, v170
	s_lshl_b32 s0, s91, 8
	s_or_b32 s34, s34, s1
	v_and_b32_e32 v0, 56, v0
	v_and_b32_e32 v131, 64, v231
	v_and_b32_e32 v130, 15, v170
	s_add_i32 s29, s0, s63
	v_lshl_add_u64 v[158:159], s[34:35], 0, v[0:1]
	v_xor_b32_e32 v0, 16, v231
	v_add_u32_e32 v131, 64, v131
	v_or_b32_e32 v160, s29, v130
	v_cmp_lt_i32_e32 vcc, v0, v131
	v_lshlrev_b64 v[176:177], 1, v[158:159]
	v_ashrrev_i32_e32 v161, 31, v160
	v_cndmask_b32_e32 v0, v231, v0, vcc
	v_lshlrev_b32_e32 v171, 2, v0
	v_xor_b32_e32 v0, 32, v231
	v_lshl_add_u64 v[162:163], s[16:17], 0, v[176:177]
	v_lshlrev_b64 v[178:179], 11, v[160:161]
	v_cmp_lt_i32_e32 vcc, v0, v131
	v_or_b32_e32 v182, s63, v130
	v_lshl_add_u64 v[130:131], v[162:163], 0, v[178:179]
	global_load_dwordx4 v[172:175], v[130:131], off nt
	global_load_dwordx4 v[154:157], v[130:131], off offset:256 nt
	v_or_b32_e32 v130, 16, v160
	v_ashrrev_i32_e32 v131, 31, v130
	v_lshlrev_b64 v[168:169], 11, v[130:131]
	v_lshl_add_u64 v[130:131], v[162:163], 0, v[168:169]
	global_load_dwordx4 v[150:153], v[130:131], off nt
	global_load_dwordx4 v[146:149], v[130:131], off offset:256 nt
	v_or_b32_e32 v130, 32, v160
	v_ashrrev_i32_e32 v131, 31, v130
	v_lshlrev_b64 v[166:167], 11, v[130:131]
	v_lshl_add_u64 v[130:131], v[162:163], 0, v[166:167]
	global_load_dwordx4 v[142:145], v[130:131], off nt
	global_load_dwordx4 v[138:141], v[130:131], off offset:256 nt
	v_or_b32_e32 v130, 48, v160
	v_ashrrev_i32_e32 v131, 31, v130
	v_lshlrev_b64 v[164:165], 11, v[130:131]
	v_lshl_add_u64 v[130:131], v[162:163], 0, v[164:165]
	global_load_dwordx4 v[134:137], v[130:131], off nt
	s_nop 0
	global_load_dwordx4 v[130:133], v[130:131], off offset:256 nt
	v_lshl_add_u64 v[178:179], s[14:15], 0, v[178:179]
	v_lshl_add_u64 v[176:177], v[178:179], 0, v[176:177]
	v_cndmask_b32_e32 v0, v231, v0, vcc
	v_lshlrev_b32_e32 v0, 2, v0
	s_lshl_b32 s1, s62, 2
	v_cmp_gt_u32_e32 vcc, 16, v170
	s_waitcnt vmcnt(0)
	v_lshlrev_b32_e32 v180, 16, v172
	v_and_b32_e32 v181, 0xffff0000, v172
	v_lshlrev_b32_e32 v172, 16, v173
	v_and_b32_e32 v173, 0xffff0000, v173
	v_pk_add_f32 v[128:129], v[128:129], v[172:173]
	v_lshlrev_b32_e32 v172, 16, v174
	v_and_b32_e32 v173, 0xffff0000, v174
	v_pk_add_f32 v[172:173], v[122:123], v[172:173]
	v_lshlrev_b32_e32 v122, 16, v175
	v_and_b32_e32 v123, 0xffff0000, v175
	v_pk_add_f32 v[126:127], v[126:127], v[180:181]
	v_pk_add_f32 v[174:175], v[124:125], v[122:123]
	v_cvt_pk_bf16_f32 v122, v126, v127
	v_cvt_pk_bf16_f32 v123, v128, v129
	v_cvt_pk_bf16_f32 v124, v172, v173
	v_cvt_pk_bf16_f32 v125, v174, v175
	global_store_dwordx4 v[176:177], v[122:125], off sc1
	s_nop 1
	v_pk_mul_f32 v[122:123], v[126:127], v[126:127]
	v_pk_mul_f32 v[126:127], v[172:173], v[172:173]
	v_lshlrev_b32_e32 v172, 16, v154
	v_and_b32_e32 v173, 0xffff0000, v154
	v_lshlrev_b32_e32 v154, 16, v155
	v_and_b32_e32 v155, 0xffff0000, v155
	v_pk_add_f32 v[120:121], v[120:121], v[154:155]
	v_lshlrev_b32_e32 v154, 16, v156
	v_and_b32_e32 v155, 0xffff0000, v156
	v_pk_add_f32 v[154:155], v[114:115], v[154:155]
	v_lshlrev_b32_e32 v114, 16, v157
	v_and_b32_e32 v115, 0xffff0000, v157
	v_pk_add_f32 v[118:119], v[118:119], v[172:173]
	v_pk_add_f32 v[156:157], v[116:117], v[114:115]
	v_cvt_pk_bf16_f32 v114, v118, v119
	v_cvt_pk_bf16_f32 v115, v120, v121
	v_cvt_pk_bf16_f32 v116, v154, v155
	v_cvt_pk_bf16_f32 v117, v156, v157
	global_store_dwordx4 v[176:177], v[114:117], off offset:256 sc1
	v_pk_mul_f32 v[124:125], v[128:129], v[128:129]
	v_pk_mul_f32 v[128:129], v[174:175], v[174:175]
	v_pk_mul_f32 v[114:115], v[118:119], v[118:119]
	v_pk_mul_f32 v[116:117], v[120:121], v[120:121]
	v_add_f32_e32 v114, v114, v115
	v_add_f32_e32 v116, v116, v117
	v_pk_mul_f32 v[118:119], v[154:155], v[154:155]
	v_pk_mul_f32 v[120:121], v[156:157], v[156:157]
	v_add_f32_e32 v114, v114, v116
	v_add_f32_e32 v115, v128, v129
	v_add_f32_e32 v116, v126, v127
	v_add_f32_e32 v120, v120, v121
	v_add_f32_e32 v118, v118, v119
	v_add_f32_e32 v115, v116, v115
	v_add_f32_e32 v116, v124, v125
	v_add_f32_e32 v117, v122, v123
	v_add_f32_e32 v118, v118, v120
	v_add_f32_e32 v116, v117, v116
	v_add_f32_e32 v114, v114, v118
	v_add_f32_e32 v115, v116, v115
	v_add_f32_e32 v114, v115, v114
	ds_bpermute_b32 v115, v171, v114
	s_waitcnt lgkmcnt(0)
	v_add_f32_e32 v115, v114, v115
	ds_bpermute_b32 v116, v0, v115
	v_lshl_or_b32 v114, v182, 4, s1
	s_and_saveexec_b64 s[16:17], vcc
	s_cbranch_execz .LBB0_107
	s_waitcnt lgkmcnt(0)
	v_add_f32_e32 v115, v115, v116
	ds_write_b32 v114, v115

.LBB0_113:
	s_or_b64 exec, exec, s[16:17]
	s_waitcnt lgkmcnt(0)
	v_lshlrev_b64 v[66:67], 11, v[160:161]
	v_lshl_add_u64 v[104:105], v[66:67], 0, s[20:21]
	v_lshl_add_u64 v[68:69], v[162:163], 0, v[104:105]
	global_load_dwordx4 v[96:99], v[68:69], off nt
	global_load_dwordx4 v[100:103], v[68:69], off offset:256 nt
	s_mov_b64 s[16:17], 0x48000
	v_lshl_add_u64 v[94:95], v[66:67], 0, s[16:17]
	s_mov_b64 s[16:17], 0x58000
	v_lshl_add_u64 v[68:69], v[162:163], 0, v[94:95]
	v_lshl_add_u64 v[92:93], v[66:67], 0, s[22:23]
	v_lshl_add_u64 v[90:91], v[66:67], 0, s[16:17]
	global_load_dwordx4 v[86:89], v[68:69], off nt
	global_load_dwordx4 v[82:85], v[68:69], off offset:256 nt
	v_lshl_add_u64 v[68:69], v[162:163], 0, v[92:93]
	v_lshl_add_u64 v[66:67], v[162:163], 0, v[90:91]
	global_load_dwordx4 v[78:81], v[68:69], off nt
	global_load_dwordx4 v[74:77], v[68:69], off offset:256 nt
	global_load_dwordx4 v[70:73], v[66:67], off nt
	s_nop 0
	global_load_dwordx4 v[66:69], v[66:67], off offset:256 nt
	v_lshl_add_u64 v[104:105], s[14:15], 0, v[104:105]
	v_lshl_add_u64 v[104:105], v[158:159], 1, v[104:105]
	s_waitcnt vmcnt(7)
	v_lshlrev_b32_e32 v106, 16, v96
	v_and_b32_e32 v107, 0xffff0000, v96
	v_lshlrev_b32_e32 v96, 16, v97
	v_and_b32_e32 v97, 0xffff0000, v97
	v_pk_add_f32 v[64:65], v[64:65], v[96:97]
	v_lshlrev_b32_e32 v96, 16, v98
	v_and_b32_e32 v97, 0xffff0000, v98
	v_pk_add_f32 v[96:97], v[58:59], v[96:97]
	v_lshlrev_b32_e32 v58, 16, v99
	v_and_b32_e32 v59, 0xffff0000, v99
	v_pk_add_f32 v[62:63], v[62:63], v[106:107]
	v_pk_add_f32 v[98:99], v[60:61], v[58:59]
	v_cvt_pk_bf16_f32 v58, v62, v63
	v_cvt_pk_bf16_f32 v59, v64, v65
	v_cvt_pk_bf16_f32 v60, v96, v97
	v_cvt_pk_bf16_f32 v61, v98, v99
	global_store_dwordx4 v[104:105], v[58:61], off sc1
	s_nop 1
	v_pk_mul_f32 v[58:59], v[62:63], v[62:63]
	v_pk_mul_f32 v[62:63], v[96:97], v[96:97]
	s_waitcnt vmcnt(7)
	v_lshlrev_b32_e32 v96, 16, v100
	v_and_b32_e32 v97, 0xffff0000, v100
	v_pk_add_f32 v[54:55], v[54:55], v[96:97]
	v_lshlrev_b32_e32 v96, 16, v101
	v_and_b32_e32 v97, 0xffff0000, v101
	v_pk_add_f32 v[56:57], v[56:57], v[96:97]
	v_lshlrev_b32_e32 v96, 16, v102
	v_and_b32_e32 v97, 0xffff0000, v102
	v_pk_add_f32 v[96:97], v[50:51], v[96:97]
	v_lshlrev_b32_e32 v50, 16, v103
	v_and_b32_e32 v51, 0xffff0000, v103
	v_pk_mul_f32 v[60:61], v[64:65], v[64:65]
	v_pk_mul_f32 v[64:65], v[98:99], v[98:99]
	v_pk_add_f32 v[98:99], v[52:53], v[50:51]
	v_cvt_pk_bf16_f32 v50, v54, v55
	v_cvt_pk_bf16_f32 v51, v56, v57
	v_cvt_pk_bf16_f32 v52, v96, v97
	v_cvt_pk_bf16_f32 v53, v98, v99
	global_store_dwordx4 v[104:105], v[50:53], off offset:256 sc1
	s_nop 1
	v_pk_mul_f32 v[50:51], v[54:55], v[54:55]
	v_pk_mul_f32 v[52:53], v[56:57], v[56:57]
	v_add_f32_e32 v50, v50, v51
	v_add_f32_e32 v52, v52, v53
	v_pk_mul_f32 v[54:55], v[96:97], v[96:97]
	v_pk_mul_f32 v[56:57], v[98:99], v[98:99]
	v_add_f32_e32 v50, v50, v52
	v_add_f32_e32 v51, v64, v65
	v_add_f32_e32 v52, v62, v63
	v_add_f32_e32 v56, v56, v57
	v_add_f32_e32 v54, v54, v55
	v_add_f32_e32 v51, v52, v51
	v_add_f32_e32 v52, v60, v61
	v_add_f32_e32 v53, v58, v59
	v_add_f32_e32 v54, v54, v56
	v_add_f32_e32 v52, v53, v52
	v_add_f32_e32 v50, v50, v54
	v_add_f32_e32 v51, v52, v51
	v_add_f32_e32 v50, v51, v50
	ds_bpermute_b32 v51, v171, v50
	s_waitcnt lgkmcnt(0)
	v_add_f32_e32 v50, v50, v51
	ds_bpermute_b32 v51, v0, v50
	s_and_saveexec_b64 s[16:17], vcc
	s_cbranch_execz .LBB0_115
	s_waitcnt lgkmcnt(0)
	v_add_f32_e32 v50, v50, v51
	ds_write_b32 v114, v50 offset:2048

.LBB0_360:
	s_mov_b32 s29, -1
	s_ashr_i32 s37, s36, 31
	v_mbcnt_lo_u32_b32 v0, s29, 0
	v_mbcnt_hi_u32_b32 v0, s29, v0
	s_lshl_b64 s[36:37], s[36:37], 7
	v_lshrrev_b32_e32 v46, 1, v0
	s_or_b64 s[36:37], s[36:37], s[80:81]
	v_and_b32_e32 v46, 56, v46
	v_mov_b32_e32 v47, v1
	v_lshl_add_u64 v[182:183], s[36:37], 0, v[46:47]
	v_lshlrev_b64 v[46:47], 2, v[182:183]
	v_lshl_add_u64 v[50:51], s[46:47], 0, v[46:47]
	v_lshl_add_u64 v[58:59], s[52:53], 0, v[46:47]
	v_lshl_add_u64 v[62:63], s[54:55], 0, v[46:47]
	v_lshl_add_u64 v[86:87], s[48:49], 0, v[46:47]
	global_load_dwordx4 v[46:49], v[50:51], off offset:16 nt
	global_load_dwordx4 v[74:77], v[50:51], off nt
	s_nop 0
	global_load_dwordx4 v[50:53], v[58:59], off offset:16 nt
	global_load_dwordx4 v[78:81], v[58:59], off nt
	s_nop 0
	global_load_dwordx4 v[58:61], v[62:63], off offset:16 nt
	global_load_dwordx4 v[82:85], v[62:63], off nt
	s_nop 0
	global_load_dwordx4 v[62:65], v[86:87], off offset:16 nt
	s_nop 0
	global_load_dwordx4 v[86:89], v[86:87], off nt
	s_waitcnt vmcnt(0)
	v_ffbh_u32_e32 v192, v191
	v_min_u32_e32 v192, 32, v192
	v_lshlrev_b64 v[190:191], v192, v[190:191]
	v_min_u32_e32 v190, 1, v190
	v_or_b32_e32 v190, v191, v190
	v_ffbh_u32_e32 v191, v189
	v_min_u32_e32 v191, 32, v191
	v_lshlrev_b64 v[188:189], v191, v[188:189]
	v_min_u32_e32 v188, 1, v188
	v_cvt_f32_u32_e32 v190, v190
	v_or_b32_e32 v188, v189, v188
	v_cvt_f32_u32_e32 v188, v188
	v_sub_u32_e32 v189, 32, v192
	v_ldexp_f32 v189, v190, v189
	v_sub_u32_e32 v190, 32, v191
	v_ldexp_f32 v188, v188, v190
	s_mov_b32 s36, 0x32800000
	v_pk_fma_f32 v[192:193], v[188:189], s[36:37], v[196:197] op_sel_hi:[1,0,0]
	s_lshl_b32 s29, s38, 8
	v_mul_f32_e32 v188, 0x4b800000, v193
	v_cmp_gt_f32_e64 s[36:37], s96, v193
	v_readlane_b32 s39, v253, 47
	s_add_i32 s29, s29, s39
	v_cndmask_b32_e64 v188, v193, v188, s[36:37]
	v_rsq_f32_e32 v188, v188
	s_ashr_i32 s39, s38, 31
	v_and_b32_e32 v0, 15, v0
	v_cmp_gt_f32_e32 vcc, s96, v192
	v_mul_f32_e32 v189, 0x45800000, v188
	v_cndmask_b32_e64 v194, v188, v189, s[36:37]
	s_lshl_b64 s[36:37], s[38:39], 2
	s_add_u32 s66, s36, s85
	v_pk_mul_f32 v[188:189], v[194:195], v[160:161] op_sel_hi:[0,1]
	v_pk_mul_f32 v[190:191], v[194:195], v[158:159] op_sel_hi:[0,1]
	v_pk_mul_f32 v[158:159], v[194:195], v[156:157] op_sel_hi:[0,1]
	v_pk_mul_f32 v[160:161], v[194:195], v[154:155] op_sel_hi:[0,1]
	v_or_b32_e32 v193, s29, v0
	s_addc_u32 s67, s37, s84
	v_cmp_lt_u32_e64 s[36:37], 1, v0
	v_mov_b32_dpp v202, v190 row_shr:1 row_mask:0xf bank_mask:0xf bound_ctrl:1
	v_mov_b32_dpp v204, v190 row_shr:2 row_mask:0xf bank_mask:0xf bound_ctrl:1
	v_mov_b32_dpp v203, v191 row_shr:1 row_mask:0xf bank_mask:0xf bound_ctrl:1
	v_mov_b32_dpp v205, v191 row_shr:2 row_mask:0xf bank_mask:0xf bound_ctrl:1
	v_mov_b32_dpp v206, v188 row_shr:1 row_mask:0xf bank_mask:0xf bound_ctrl:1
	v_mov_b32_dpp v208, v188 row_shr:2 row_mask:0xf bank_mask:0xf bound_ctrl:1
	v_mov_b32_dpp v207, v189 row_shr:1 row_mask:0xf bank_mask:0xf bound_ctrl:1
	v_mov_b32_dpp v209, v189 row_shr:2 row_mask:0xf bank_mask:0xf bound_ctrl:1
	v_mov_b32_dpp v210, v160 row_shr:1 row_mask:0xf bank_mask:0xf bound_ctrl:1
	v_mov_b32_dpp v212, v160 row_shr:2 row_mask:0xf bank_mask:0xf bound_ctrl:1
	v_mov_b32_dpp v211, v161 row_shr:1 row_mask:0xf bank_mask:0xf bound_ctrl:1
	v_mov_b32_dpp v213, v161 row_shr:2 row_mask:0xf bank_mask:0xf bound_ctrl:1
	v_mov_b32_dpp v214, v158 row_shr:1 row_mask:0xf bank_mask:0xf bound_ctrl:1
	v_mov_b32_dpp v216, v158 row_shr:2 row_mask:0xf bank_mask:0xf bound_ctrl:1
	v_mov_b32_dpp v215, v159 row_shr:1 row_mask:0xf bank_mask:0xf bound_ctrl:1
	v_mov_b32_dpp v217, v159 row_shr:2 row_mask:0xf bank_mask:0xf bound_ctrl:1
	s_and_saveexec_b64 s[38:39], s[36:37]
	s_xor_b64 s[38:39], exec, s[38:39]
	s_cbranch_execz .LBB0_362
	v_pk_fma_f32 v[154:155], v[48:49], v[216:217], v[64:65]
	v_pk_fma_f32 v[212:213], v[46:47], v[212:213], v[62:63]
	v_pk_fma_f32 v[154:155], v[52:53], v[214:215], v[154:155]
	v_pk_fma_f32 v[210:211], v[50:51], v[210:211], v[212:213]
	v_pk_fma_f32 v[154:155], v[158:159], v[60:61], v[154:155]
	v_pk_fma_f32 v[210:211], v[160:161], v[58:59], v[210:211]
	v_mul_f32_e32 v156, 0x3d372713, v154
	v_mul_f32_e32 v157, 0x3d372713, v155
	v_pk_mul_f32 v[200:201], v[194:195], v[148:149] op_sel_hi:[0,1]
	v_mul_f32_e32 v195, 0x3d372713, v210
	v_mul_f32_e32 v156, v154, v156
	v_mul_f32_e32 v157, v155, v157
	v_mul_f32_e32 v195, v210, v195
	v_mul_f32_e32 v212, 0x3d372713, v211
	v_fma_f32 v156, v154, v156, v154
	v_fma_f32 v157, v155, v157, v155
	v_fma_f32 v195, v210, v195, v210
	v_mul_f32_e32 v212, v211, v212
	v_mul_f32_e32 v156, 0xc0135761, v156
	v_mul_f32_e32 v157, 0xc0135761, v157
	v_mul_f32_e32 v195, 0xc0135761, v195
	v_fma_f32 v212, v211, v212, v211
	v_exp_f32_e32 v156, v156
	v_exp_f32_e32 v157, v157
	v_exp_f32_e32 v195, v195
	v_mul_f32_e32 v212, 0xc0135761, v212
	v_exp_f32_e32 v213, v212
	v_add_f32_e32 v156, 1.0, v156
	v_add_f32_e32 v157, 1.0, v157
	v_add_f32_e32 v195, 1.0, v195
	v_rcp_f32_e32 v156, v156
	v_rcp_f32_e32 v157, v157
	v_rcp_f32_e32 v212, v195
	v_add_f32_e32 v195, 1.0, v213
	v_rcp_f32_e32 v213, v195
	v_pk_mul_f32 v[154:155], v[154:155], v[156:157]
	v_pk_fma_f32 v[204:205], v[74:75], v[204:205], v[86:87]
	v_pk_mul_f32 v[200:201], v[200:201], v[154:155]
	v_pk_mul_f32 v[154:155], v[194:195], v[146:147] op_sel_hi:[0,1]
	v_pk_mul_f32 v[156:157], v[210:211], v[212:213]
	v_pk_fma_f32 v[202:203], v[78:79], v[202:203], v[204:205]
	v_pk_mul_f32 v[156:157], v[154:155], v[156:157]
	v_pk_fma_f32 v[154:155], v[76:77], v[208:209], v[88:89]
	v_pk_fma_f32 v[202:203], v[190:191], v[82:83], v[202:203]
	v_pk_fma_f32 v[154:155], v[80:81], v[206:207], v[154:155]
	v_mul_f32_e32 v204, 0x3d372713, v202
	v_pk_fma_f32 v[154:155], v[188:189], v[84:85], v[154:155]
	v_mul_f32_e32 v204, v202, v204
	v_mul_f32_e32 v195, 0x3d372713, v154
	v_mul_f32_e32 v195, v154, v195
	v_mul_f32_e32 v206, 0x3d372713, v155
	v_fma_f32 v195, v154, v195, v154
	v_mul_f32_e32 v206, v155, v206
	v_mul_f32_e32 v195, 0xc0135761, v195
	v_fma_f32 v206, v155, v206, v155
	v_mul_f32_e32 v205, 0x3d372713, v203
	v_exp_f32_e32 v195, v195
	v_mul_f32_e32 v206, 0xc0135761, v206
	v_fma_f32 v204, v202, v204, v202
	v_mul_f32_e32 v205, v203, v205
	v_exp_f32_e32 v207, v206
	v_mul_f32_e32 v204, 0xc0135761, v204
	v_fma_f32 v205, v203, v205, v203
	v_exp_f32_e32 v204, v204
	v_mul_f32_e32 v205, 0xc0135761, v205
	v_exp_f32_e32 v205, v205
	v_add_f32_e32 v195, 1.0, v195
	v_rcp_f32_e32 v206, v195
	v_pk_mul_f32 v[208:209], v[194:195], v[152:153] op_sel_hi:[0,1]
	v_add_f32_e32 v195, 1.0, v207
	v_rcp_f32_e32 v207, v195
	v_add_f32_e32 v195, 1.0, v204
	v_rcp_f32_e32 v204, v195
	v_add_f32_e32 v195, 1.0, v205
	v_rcp_f32_e32 v205, v195
	v_pk_mul_f32 v[154:155], v[154:155], v[206:207]
	v_cvt_pk_bf16_f32 v156, v156, v157
	v_pk_mul_f32 v[206:207], v[208:209], v[154:155]
	v_pk_mul_f32 v[154:155], v[194:195], v[150:151] op_sel_hi:[0,1]
	v_pk_mul_f32 v[194:195], v[202:203], v[204:205]
	v_cvt_pk_bf16_f32 v157, v200, v201
	v_pk_mul_f32 v[154:155], v[154:155], v[194:195]
	v_mov_b64_e32 v[194:195], s[16:17]
	v_cvt_pk_bf16_f32 v154, v154, v155
	v_cvt_pk_bf16_f32 v155, v206, v207
	v_mad_i64_i32 v[200:201], s[40:41], v193, s2, v[194:195]

.LBB0_404:
	s_mov_b32 s0, -1
	s_add_u32 s14, s74, 0x2200000
	s_waitcnt vmcnt(0)
	s_barrier
	s_addc_u32 s15, s75, 0
	v_mbcnt_lo_u32_b32 v0, s0, 0
	v_mbcnt_hi_u32_b32 v166, s0, v0
	s_lshl_b32 s0, s88, 8
	v_and_b32_e32 v130, 15, v166
	s_add_i32 s17, s0, s63
	v_or_b32_e32 v156, s17, v130
	s_ashr_i32 s17, s16, 31
	s_lshl_b32 s1, s62, 5
	s_lshl_b64 s[16:17], s[16:17], 8
	v_lshrrev_b32_e32 v0, 1, v166
	s_or_b32 s16, s16, s1
	v_and_b32_e32 v0, 56, v0
	v_and_b32_e32 v131, 64, v231
	v_lshl_add_u64 v[154:155], s[16:17], 0, v[0:1]
	v_xor_b32_e32 v0, 16, v231
	v_add_u32_e32 v131, 64, v131
	v_cmp_lt_i32_e32 vcc, v0, v131
	v_lshlrev_b64 v[178:179], 1, v[154:155]
	s_mov_b64 s[16:17], 0x8800000
	v_cndmask_b32_e32 v0, v231, v0, vcc
	v_lshlrev_b32_e32 v168, 2, v0
	v_xor_b32_e32 v0, 32, v231
	v_cmp_lt_i32_e32 vcc, v0, v131
	v_ashrrev_i32_e32 v157, 31, v156
	v_lshlrev_b64 v[180:181], 11, v[156:157]
	v_cndmask_b32_e32 v0, v231, v0, vcc
	v_lshlrev_b32_e32 v167, 2, v0
	v_or_b32_e32 v0, s63, v130
	v_lshl_add_u64 v[130:131], s[74:75], 0, v[178:179]
	v_lshl_add_u64 v[158:159], v[130:131], 0, s[16:17]
	v_lshl_add_u64 v[130:131], v[158:159], 0, v[180:181]
	global_load_dwordx4 v[170:173], v[130:131], off nt
	global_load_dwordx4 v[174:177], v[130:131], off offset:256 nt
	v_or_b32_e32 v130, 16, v156
	v_ashrrev_i32_e32 v131, 31, v130
	v_lshlrev_b64 v[164:165], 11, v[130:131]
	v_lshl_add_u64 v[130:131], v[158:159], 0, v[164:165]
	global_load_dwordx4 v[150:153], v[130:131], off nt
	global_load_dwordx4 v[146:149], v[130:131], off offset:256 nt
	v_or_b32_e32 v130, 32, v156
	v_ashrrev_i32_e32 v131, 31, v130
	v_lshlrev_b64 v[162:163], 11, v[130:131]
	v_lshl_add_u64 v[130:131], v[158:159], 0, v[162:163]
	global_load_dwordx4 v[142:145], v[130:131], off nt
	global_load_dwordx4 v[138:141], v[130:131], off offset:256 nt
	v_or_b32_e32 v130, 48, v156
	v_ashrrev_i32_e32 v131, 31, v130
	v_lshlrev_b64 v[160:161], 11, v[130:131]
	v_lshl_add_u64 v[130:131], v[158:159], 0, v[160:161]
	global_load_dwordx4 v[134:137], v[130:131], off nt
	s_nop 0
	global_load_dwordx4 v[130:133], v[130:131], off offset:256 nt
	v_lshl_add_u64 v[180:181], s[14:15], 0, v[180:181]
	v_lshl_add_u64 v[178:179], v[180:181], 0, v[178:179]
	v_cmp_gt_u32_e32 vcc, 16, v166
	s_lshl_b32 s1, s62, 2
	s_waitcnt vmcnt(0)
	v_lshlrev_b32_e32 v182, 16, v170
	v_and_b32_e32 v183, 0xffff0000, v170
	v_lshlrev_b32_e32 v170, 16, v171
	v_and_b32_e32 v171, 0xffff0000, v171
	v_pk_add_f32 v[128:129], v[128:129], v[170:171]
	v_lshlrev_b32_e32 v170, 16, v172
	v_and_b32_e32 v171, 0xffff0000, v172
	v_pk_add_f32 v[170:171], v[122:123], v[170:171]
	v_lshlrev_b32_e32 v122, 16, v173
	v_and_b32_e32 v123, 0xffff0000, v173
	v_pk_add_f32 v[126:127], v[126:127], v[182:183]
	v_pk_add_f32 v[172:173], v[124:125], v[122:123]
	v_cvt_pk_bf16_f32 v122, v126, v127
	v_cvt_pk_bf16_f32 v123, v128, v129
	v_cvt_pk_bf16_f32 v124, v170, v171
	v_cvt_pk_bf16_f32 v125, v172, v173
	global_store_dwordx4 v[178:179], v[122:125], off sc1
	s_nop 1
	v_pk_mul_f32 v[122:123], v[126:127], v[126:127]
	v_pk_mul_f32 v[126:127], v[170:171], v[170:171]
	v_lshlrev_b32_e32 v170, 16, v174
	v_and_b32_e32 v171, 0xffff0000, v174
	v_pk_add_f32 v[118:119], v[118:119], v[170:171]
	v_lshlrev_b32_e32 v170, 16, v175
	v_and_b32_e32 v171, 0xffff0000, v175
	v_pk_add_f32 v[120:121], v[120:121], v[170:171]
	v_lshlrev_b32_e32 v170, 16, v176
	v_and_b32_e32 v171, 0xffff0000, v176
	v_pk_add_f32 v[170:171], v[114:115], v[170:171]
	v_lshlrev_b32_e32 v114, 16, v177
	v_and_b32_e32 v115, 0xffff0000, v177
	v_pk_mul_f32 v[124:125], v[128:129], v[128:129]
	v_pk_mul_f32 v[128:129], v[172:173], v[172:173]
	v_pk_add_f32 v[172:173], v[116:117], v[114:115]
	v_cvt_pk_bf16_f32 v114, v118, v119
	v_cvt_pk_bf16_f32 v115, v120, v121
	v_cvt_pk_bf16_f32 v116, v170, v171
	v_cvt_pk_bf16_f32 v117, v172, v173
	global_store_dwordx4 v[178:179], v[114:117], off offset:256 sc1
	s_nop 1
	v_pk_mul_f32 v[114:115], v[118:119], v[118:119]
	v_pk_mul_f32 v[116:117], v[120:121], v[120:121]
	v_add_f32_e32 v114, v114, v115
	v_add_f32_e32 v116, v116, v117
	v_pk_mul_f32 v[118:119], v[170:171], v[170:171]
	v_pk_mul_f32 v[120:121], v[172:173], v[172:173]
	v_add_f32_e32 v114, v114, v116
	v_add_f32_e32 v115, v128, v129
	v_add_f32_e32 v116, v126, v127
	v_add_f32_e32 v120, v120, v121
	v_add_f32_e32 v118, v118, v119
	v_add_f32_e32 v115, v116, v115
	v_add_f32_e32 v116, v124, v125
	v_add_f32_e32 v117, v122, v123
	v_add_f32_e32 v118, v118, v120
	v_add_f32_e32 v116, v117, v116
	v_add_f32_e32 v114, v114, v118
	v_add_f32_e32 v115, v116, v115
	v_add_f32_e32 v114, v115, v114
	ds_bpermute_b32 v115, v168, v114
	s_waitcnt lgkmcnt(0)
	v_add_f32_e32 v114, v114, v115
	ds_bpermute_b32 v115, v167, v114
	s_and_saveexec_b64 s[16:17], vcc
	s_cbranch_execz .LBB0_406
	v_lshl_or_b32 v116, v0, 4, s1
	s_waitcnt lgkmcnt(0)
	v_add_f32_e32 v114, v114, v115
	ds_write_b32 v116, v114

.LBB0_412:
	s_or_b64 exec, exec, s[16:17]
	s_waitcnt lgkmcnt(0)
	v_lshlrev_b64 v[66:67], 11, v[156:157]
	v_lshl_add_u64 v[104:105], v[66:67], 0, s[20:21]
	v_lshl_add_u64 v[68:69], v[158:159], 0, v[104:105]
	global_load_dwordx4 v[96:99], v[68:69], off nt
	global_load_dwordx4 v[100:103], v[68:69], off offset:256 nt
	s_mov_b64 s[16:17], 0x48000
	v_lshl_add_u64 v[94:95], v[66:67], 0, s[16:17]
	s_mov_b64 s[16:17], 0x58000
	v_lshl_add_u64 v[68:69], v[158:159], 0, v[94:95]
	v_lshl_add_u64 v[92:93], v[66:67], 0, s[22:23]
	v_lshl_add_u64 v[90:91], v[66:67], 0, s[16:17]
	global_load_dwordx4 v[86:89], v[68:69], off nt
	global_load_dwordx4 v[82:85], v[68:69], off offset:256 nt
	v_lshl_add_u64 v[68:69], v[158:159], 0, v[92:93]
	v_lshl_add_u64 v[66:67], v[158:159], 0, v[90:91]
	global_load_dwordx4 v[78:81], v[68:69], off nt
	global_load_dwordx4 v[74:77], v[68:69], off offset:256 nt
	global_load_dwordx4 v[70:73], v[66:67], off nt
	s_nop 0
	global_load_dwordx4 v[66:69], v[66:67], off offset:256 nt
	v_lshl_add_u64 v[104:105], s[14:15], 0, v[104:105]
	v_lshl_add_u64 v[104:105], v[154:155], 1, v[104:105]
	s_waitcnt vmcnt(7)
	v_lshlrev_b32_e32 v106, 16, v96
	v_and_b32_e32 v107, 0xffff0000, v96
	v_lshlrev_b32_e32 v96, 16, v97
	v_and_b32_e32 v97, 0xffff0000, v97
	v_pk_add_f32 v[64:65], v[64:65], v[96:97]
	v_lshlrev_b32_e32 v96, 16, v98
	v_and_b32_e32 v97, 0xffff0000, v98
	v_pk_add_f32 v[96:97], v[58:59], v[96:97]
	v_lshlrev_b32_e32 v58, 16, v99
	v_and_b32_e32 v59, 0xffff0000, v99
	v_pk_add_f32 v[62:63], v[62:63], v[106:107]
	v_pk_add_f32 v[98:99], v[60:61], v[58:59]
	v_cvt_pk_bf16_f32 v58, v62, v63
	v_cvt_pk_bf16_f32 v59, v64, v65
	v_cvt_pk_bf16_f32 v60, v96, v97
	v_cvt_pk_bf16_f32 v61, v98, v99
	global_store_dwordx4 v[104:105], v[58:61], off sc1
	s_nop 1
	v_pk_mul_f32 v[58:59], v[62:63], v[62:63]
	v_pk_mul_f32 v[62:63], v[96:97], v[96:97]
	s_waitcnt vmcnt(7)
	v_lshlrev_b32_e32 v96, 16, v100
	v_and_b32_e32 v97, 0xffff0000, v100
	v_pk_add_f32 v[54:55], v[54:55], v[96:97]
	v_lshlrev_b32_e32 v96, 16, v101
	v_and_b32_e32 v97, 0xffff0000, v101
	v_pk_add_f32 v[56:57], v[56:57], v[96:97]
	v_lshlrev_b32_e32 v96, 16, v102
	v_and_b32_e32 v97, 0xffff0000, v102
	v_pk_add_f32 v[96:97], v[50:51], v[96:97]
	v_lshlrev_b32_e32 v50, 16, v103
	v_and_b32_e32 v51, 0xffff0000, v103
	v_pk_mul_f32 v[60:61], v[64:65], v[64:65]
	v_pk_mul_f32 v[64:65], v[98:99], v[98:99]
	v_pk_add_f32 v[98:99], v[52:53], v[50:51]
	v_cvt_pk_bf16_f32 v50, v54, v55
	v_cvt_pk_bf16_f32 v51, v56, v57
	v_cvt_pk_bf16_f32 v52, v96, v97
	v_cvt_pk_bf16_f32 v53, v98, v99
	global_store_dwordx4 v[104:105], v[50:53], off offset:256 sc1
	s_nop 1
	v_pk_mul_f32 v[50:51], v[54:55], v[54:55]
	v_pk_mul_f32 v[52:53], v[56:57], v[56:57]
	v_add_f32_e32 v50, v50, v51
	v_add_f32_e32 v52, v52, v53
	v_pk_mul_f32 v[54:55], v[96:97], v[96:97]
	v_pk_mul_f32 v[56:57], v[98:99], v[98:99]
	v_add_f32_e32 v50, v50, v52
	v_add_f32_e32 v51, v64, v65
	v_add_f32_e32 v52, v62, v63
	v_add_f32_e32 v56, v56, v57
	v_add_f32_e32 v54, v54, v55
	v_add_f32_e32 v51, v52, v51
	v_add_f32_e32 v52, v60, v61
	v_add_f32_e32 v53, v58, v59
	v_add_f32_e32 v54, v54, v56
	v_add_f32_e32 v52, v53, v52
	v_add_f32_e32 v50, v50, v54
	v_add_f32_e32 v51, v52, v51
	v_add_f32_e32 v50, v51, v50
	ds_bpermute_b32 v51, v168, v50
	s_waitcnt lgkmcnt(0)
	v_add_f32_e32 v50, v50, v51
	ds_bpermute_b32 v51, v167, v50
	s_and_saveexec_b64 s[16:17], vcc
	s_cbranch_execz .LBB0_414
	v_lshl_or_b32 v52, v0, 4, s1
	s_waitcnt lgkmcnt(0)
	v_add_f32_e32 v50, v50, v51
	ds_write_b32 v52, v50 offset:2048

.LBB0_503:
	s_mov_b32 s0, -1
	s_add_u32 s14, s74, 0x8800000
	s_waitcnt vmcnt(0)
	s_barrier
	s_addc_u32 s15, s75, 0
	v_mbcnt_lo_u32_b32 v0, s0, 0
	v_mbcnt_hi_u32_b32 v166, s0, v0
	s_lshl_b32 s0, s90, 8
	v_and_b32_e32 v130, 15, v166
	s_add_i32 s17, s0, s65
	v_or_b32_e32 v156, s17, v130
	s_ashr_i32 s17, s16, 31
	s_lshl_b32 s1, s64, 5
	s_lshl_b64 s[16:17], s[16:17], 8
	v_lshrrev_b32_e32 v0, 1, v166
	s_or_b32 s16, s16, s1
	v_and_b32_e32 v0, 56, v0
	v_and_b32_e32 v131, 64, v231
	v_lshl_add_u64 v[154:155], s[16:17], 0, v[0:1]
	v_xor_b32_e32 v0, 16, v231
	v_add_u32_e32 v131, 64, v131
	v_cmp_lt_i32_e32 vcc, v0, v131
	v_readlane_b32 s16, v253, 34
	v_lshlrev_b64 v[178:179], 1, v[154:155]
	v_cndmask_b32_e32 v0, v231, v0, vcc
	v_lshlrev_b32_e32 v168, 2, v0
	v_xor_b32_e32 v0, 32, v231
	v_cmp_lt_i32_e32 vcc, v0, v131
	v_readlane_b32 s17, v253, 35
	v_ashrrev_i32_e32 v157, 31, v156
	v_cndmask_b32_e32 v0, v231, v0, vcc
	v_lshl_add_u64 v[158:159], s[16:17], 0, v[178:179]
	v_lshlrev_b64 v[180:181], 11, v[156:157]
	v_lshlrev_b32_e32 v167, 2, v0
	v_or_b32_e32 v0, s65, v130
	v_lshl_add_u64 v[130:131], v[158:159], 0, v[180:181]
	global_load_dwordx4 v[170:173], v[130:131], off nt
	global_load_dwordx4 v[174:177], v[130:131], off offset:256 nt
	v_or_b32_e32 v130, 16, v156
	v_ashrrev_i32_e32 v131, 31, v130
	v_lshlrev_b64 v[164:165], 11, v[130:131]
	v_lshl_add_u64 v[130:131], v[158:159], 0, v[164:165]
	global_load_dwordx4 v[150:153], v[130:131], off nt
	global_load_dwordx4 v[146:149], v[130:131], off offset:256 nt
	v_or_b32_e32 v130, 32, v156
	v_ashrrev_i32_e32 v131, 31, v130
	v_lshlrev_b64 v[162:163], 11, v[130:131]
	v_lshl_add_u64 v[130:131], v[158:159], 0, v[162:163]
	global_load_dwordx4 v[142:145], v[130:131], off nt
	global_load_dwordx4 v[138:141], v[130:131], off offset:256 nt
	v_or_b32_e32 v130, 48, v156
	v_ashrrev_i32_e32 v131, 31, v130
	v_lshlrev_b64 v[160:161], 11, v[130:131]
	v_lshl_add_u64 v[130:131], v[158:159], 0, v[160:161]
	global_load_dwordx4 v[134:137], v[130:131], off nt
	s_nop 0
	global_load_dwordx4 v[130:133], v[130:131], off offset:256 nt
	v_lshl_add_u64 v[180:181], s[14:15], 0, v[180:181]
	v_lshl_add_u64 v[178:179], v[180:181], 0, v[178:179]
	v_cmp_gt_u32_e32 vcc, 16, v166
	s_lshl_b32 s1, s64, 2
	s_waitcnt vmcnt(0)
	v_lshlrev_b32_e32 v182, 16, v170
	v_and_b32_e32 v183, 0xffff0000, v170
	v_lshlrev_b32_e32 v170, 16, v171
	v_and_b32_e32 v171, 0xffff0000, v171
	v_pk_add_f32 v[128:129], v[128:129], v[170:171]
	v_lshlrev_b32_e32 v170, 16, v172
	v_and_b32_e32 v171, 0xffff0000, v172
	v_pk_add_f32 v[170:171], v[122:123], v[170:171]
	v_lshlrev_b32_e32 v122, 16, v173
	v_and_b32_e32 v123, 0xffff0000, v173
	v_pk_add_f32 v[126:127], v[126:127], v[182:183]
	v_pk_add_f32 v[172:173], v[124:125], v[122:123]
	v_cvt_pk_bf16_f32 v122, v126, v127
	v_cvt_pk_bf16_f32 v123, v128, v129
	v_cvt_pk_bf16_f32 v124, v170, v171
	v_cvt_pk_bf16_f32 v125, v172, v173
	global_store_dwordx4 v[178:179], v[122:125], off sc1
	s_nop 1
	v_pk_mul_f32 v[122:123], v[126:127], v[126:127]
	v_pk_mul_f32 v[126:127], v[170:171], v[170:171]
	v_lshlrev_b32_e32 v170, 16, v174
	v_and_b32_e32 v171, 0xffff0000, v174
	v_pk_add_f32 v[118:119], v[118:119], v[170:171]
	v_lshlrev_b32_e32 v170, 16, v175
	v_and_b32_e32 v171, 0xffff0000, v175
	v_pk_add_f32 v[120:121], v[120:121], v[170:171]
	v_lshlrev_b32_e32 v170, 16, v176
	v_and_b32_e32 v171, 0xffff0000, v176
	v_pk_add_f32 v[170:171], v[114:115], v[170:171]
	v_lshlrev_b32_e32 v114, 16, v177
	v_and_b32_e32 v115, 0xffff0000, v177
	v_pk_mul_f32 v[124:125], v[128:129], v[128:129]
	v_pk_mul_f32 v[128:129], v[172:173], v[172:173]
	v_pk_add_f32 v[172:173], v[116:117], v[114:115]
	v_cvt_pk_bf16_f32 v114, v118, v119
	v_cvt_pk_bf16_f32 v115, v120, v121
	v_cvt_pk_bf16_f32 v116, v170, v171
	v_cvt_pk_bf16_f32 v117, v172, v173
	global_store_dwordx4 v[178:179], v[114:117], off offset:256 sc1
	s_nop 1
	v_pk_mul_f32 v[114:115], v[118:119], v[118:119]
	v_pk_mul_f32 v[116:117], v[120:121], v[120:121]
	v_add_f32_e32 v114, v114, v115
	v_add_f32_e32 v116, v116, v117
	v_pk_mul_f32 v[118:119], v[170:171], v[170:171]
	v_pk_mul_f32 v[120:121], v[172:173], v[172:173]
	v_add_f32_e32 v114, v114, v116
	v_add_f32_e32 v115, v128, v129
	v_add_f32_e32 v116, v126, v127
	v_add_f32_e32 v120, v120, v121
	v_add_f32_e32 v118, v118, v119
	v_add_f32_e32 v115, v116, v115
	v_add_f32_e32 v116, v124, v125
	v_add_f32_e32 v117, v122, v123
	v_add_f32_e32 v118, v118, v120
	v_add_f32_e32 v116, v117, v116
	v_add_f32_e32 v114, v114, v118
	v_add_f32_e32 v115, v116, v115
	v_add_f32_e32 v114, v115, v114
	ds_bpermute_b32 v115, v168, v114
	s_waitcnt lgkmcnt(0)
	v_add_f32_e32 v114, v114, v115
	ds_bpermute_b32 v115, v167, v114
	s_and_saveexec_b64 s[16:17], vcc
	s_cbranch_execz .LBB0_505
	v_lshl_or_b32 v116, v0, 4, s1
	s_waitcnt lgkmcnt(0)
	v_add_f32_e32 v114, v114, v115
	ds_write_b32 v116, v114

.LBB0_545:
	s_mov_b32 s0, -1
	s_add_u32 s16, s74, 0x8800000
	s_waitcnt vmcnt(0)
	s_barrier
	s_addc_u32 s17, s75, 0
	v_mbcnt_lo_u32_b32 v0, s0, 0
	v_mbcnt_hi_u32_b32 v190, s0, v0
	s_lshl_b32 s14, s90, 8
	v_and_b32_e32 v193, 15, v190
	s_add_i32 s0, s14, s60
	s_ashr_i32 s37, s36, 31
	s_lshl_b32 s15, s61, 5
	v_or_b32_e32 v180, s0, v193
	s_lshl_b64 s[0:1], s[36:37], 8
	v_lshrrev_b32_e32 v0, 1, v190
	s_or_b32 s0, s0, s15
	v_and_b32_e32 v0, 56, v0
	v_lshl_add_u64 v[178:179], s[0:1], 0, v[0:1]
	v_readlane_b32 s0, v253, 47
	v_readlane_b32 s1, v253, 48
	v_ashrrev_i32_e32 v181, 31, v180
	v_lshlrev_b64 v[130:131], 12, v[180:181]
	v_lshl_add_u64 v[182:183], v[178:179], 2, s[0:1]
	v_lshl_add_u64 v[130:131], v[182:183], 0, v[130:131]
	global_load_dwordx4 v[200:203], v[130:131], off nt
	global_load_dwordx4 v[204:207], v[130:131], off offset:16 nt
	global_load_dwordx4 v[208:211], v[130:131], off offset:512 nt
	global_load_dwordx4 v[212:215], v[130:131], off offset:528 nt
	v_or_b32_e32 v188, 16, v180
	v_or_b32_e32 v186, 32, v180
	v_or_b32_e32 v184, 48, v180
	v_ashrrev_i32_e32 v189, 31, v188
	v_ashrrev_i32_e32 v187, 31, v186
	v_ashrrev_i32_e32 v185, 31, v184
	v_lshlrev_b64 v[130:131], 12, v[188:189]
	v_lshlrev_b64 v[132:133], 12, v[186:187]
	v_lshlrev_b64 v[134:135], 12, v[184:185]
	v_lshl_add_u64 v[130:131], v[182:183], 0, v[130:131]
	v_lshl_add_u64 v[132:133], v[182:183], 0, v[132:133]
	v_lshl_add_u64 v[134:135], v[182:183], 0, v[134:135]
	global_load_dwordx4 v[170:173], v[130:131], off offset:16 nt
	global_load_dwordx4 v[174:177], v[130:131], off nt
	global_load_dwordx4 v[162:165], v[130:131], off offset:528 nt
	global_load_dwordx4 v[166:169], v[130:131], off offset:512 nt
	global_load_dwordx4 v[154:157], v[132:133], off offset:16 nt
	global_load_dwordx4 v[158:161], v[132:133], off nt
	global_load_dwordx4 v[146:149], v[132:133], off offset:528 nt
	global_load_dwordx4 v[150:153], v[132:133], off offset:512 nt
	global_load_dwordx4 v[138:141], v[134:135], off offset:16 nt
	global_load_dwordx4 v[142:145], v[134:135], off nt
	s_nop 0
	global_load_dwordx4 v[130:133], v[134:135], off offset:528 nt
	s_nop 0
	global_load_dwordx4 v[134:137], v[134:135], off offset:512 nt
	v_and_b32_e32 v191, 64, v231
	v_xor_b32_e32 v0, 16, v231
	v_add_u32_e32 v191, 64, v191
	v_xor_b32_e32 v192, 32, v231
	v_cmp_lt_i32_e32 vcc, v0, v191
	v_lshlrev_b64 v[194:195], 11, v[180:181]
	s_lshl_b32 s15, s61, 2
	v_cndmask_b32_e32 v0, v231, v0, vcc
	v_cmp_lt_i32_e32 vcc, v192, v191
	s_waitcnt vmcnt(0)
	v_pk_add_f32 v[128:129], v[128:129], v[202:203]
	v_pk_add_f32 v[126:127], v[126:127], v[200:201]
	v_pk_add_f32 v[124:125], v[124:125], v[206:207]
	v_pk_add_f32 v[122:123], v[122:123], v[204:205]
	v_pk_add_f32 v[200:201], v[116:117], v[214:215]
	v_pk_add_f32 v[202:203], v[114:115], v[212:213]
	v_cvt_pk_bf16_f32 v114, v126, v127
	v_cvt_pk_bf16_f32 v115, v128, v129
	v_cvt_pk_bf16_f32 v116, v122, v123
	v_cvt_pk_bf16_f32 v117, v124, v125
	v_mul_f32_e32 v127, v127, v127
	v_mul_f32_e32 v129, v129, v129
	v_mul_f32_e32 v123, v123, v123
	v_mul_f32_e32 v125, v125, v125
	v_fmac_f32_e32 v127, v126, v126
	v_fmac_f32_e32 v129, v128, v128
	v_fmac_f32_e32 v123, v122, v122
	v_fmac_f32_e32 v125, v124, v124
	v_pk_add_f32 v[120:121], v[120:121], v[210:211]
	v_pk_add_f32 v[118:119], v[118:119], v[208:209]
	v_add_f32_e32 v122, v127, v129
	v_add_f32_e32 v123, v123, v125
	v_cndmask_b32_e32 v191, v231, v192, vcc
	v_lshlrev_b32_e32 v192, 2, v0
	v_or_b32_e32 v0, s60, v193
	v_mul_f32_e32 v181, v119, v119
	v_mul_f32_e32 v193, v121, v121
	v_mul_f32_e32 v204, v203, v203
	v_add_f32_e32 v122, v122, v123
	v_mul_f32_e32 v123, v201, v201
	v_fmac_f32_e32 v181, v118, v118
	v_fmac_f32_e32 v193, v120, v120
	v_fmac_f32_e32 v204, v202, v202
	v_fmac_f32_e32 v123, v200, v200
	v_add_f32_e32 v124, v181, v193
	v_add_f32_e32 v123, v204, v123
	v_add_f32_e32 v123, v124, v123
	v_add_f32_e32 v124, v122, v123
	ds_bpermute_b32 v125, v192, v124
	v_lshl_add_u64 v[122:123], s[16:17], 0, v[194:195]
	v_lshl_add_u64 v[122:123], v[178:179], 1, v[122:123]
	v_lshlrev_b32_e32 v191, 2, v191
	global_store_dwordx4 v[122:123], v[114:117], off sc1
	v_cmp_gt_u32_e32 vcc, 16, v190
	s_waitcnt lgkmcnt(0)
	v_add_f32_e32 v114, v124, v125
	ds_bpermute_b32 v115, v191, v114
	v_cvt_pk_bf16_f32 v116, v118, v119
	v_cvt_pk_bf16_f32 v117, v120, v121
	v_cvt_pk_bf16_f32 v118, v202, v203
	v_cvt_pk_bf16_f32 v119, v200, v201
	global_store_dwordx4 v[122:123], v[116:119], off offset:256 sc1
	s_and_saveexec_b64 s[0:1], vcc
	s_cbranch_execz .LBB0_547
	v_lshl_or_b32 v116, v0, 4, s15
	s_waitcnt lgkmcnt(0)
	v_add_f32_e32 v114, v114, v115
	ds_write_b32 v116, v114

.LBB0_553:
	s_or_b64 exec, exec, s[0:1]
	v_add_u32_e32 v136, 0x80, v180
	v_ashrrev_i32_e32 v137, 31, v136
	s_waitcnt lgkmcnt(0)
	v_lshlrev_b64 v[66:67], 12, v[136:137]
	v_lshl_add_u64 v[66:67], v[182:183], 0, v[66:67]
	global_load_dwordx4 v[120:123], v[66:67], off nt
	global_load_dwordx4 v[124:127], v[66:67], off offset:16 nt
	global_load_dwordx4 v[128:131], v[66:67], off offset:512 nt
	global_load_dwordx4 v[132:135], v[66:67], off offset:528 nt
	v_add_u32_e32 v118, 0x90, v180
	v_add_u32_e32 v116, 0xa0, v180
	v_add_u32_e32 v114, 0xb0, v180
	v_ashrrev_i32_e32 v119, 31, v118
	v_ashrrev_i32_e32 v117, 31, v116
	v_ashrrev_i32_e32 v115, 31, v114
	v_lshlrev_b64 v[66:67], 12, v[118:119]
	v_lshlrev_b64 v[68:69], 12, v[116:117]
	v_lshlrev_b64 v[70:71], 12, v[114:115]
	v_lshl_add_u64 v[66:67], v[182:183], 0, v[66:67]
	v_lshl_add_u64 v[68:69], v[182:183], 0, v[68:69]
	v_lshl_add_u64 v[70:71], v[182:183], 0, v[70:71]
	global_load_dwordx4 v[106:109], v[66:67], off offset:16 nt
	global_load_dwordx4 v[110:113], v[66:67], off nt
	global_load_dwordx4 v[98:101], v[66:67], off offset:528 nt
	global_load_dwordx4 v[102:105], v[66:67], off offset:512 nt
	global_load_dwordx4 v[90:93], v[68:69], off offset:16 nt
	global_load_dwordx4 v[94:97], v[68:69], off nt
	global_load_dwordx4 v[82:85], v[68:69], off offset:528 nt
	global_load_dwordx4 v[86:89], v[68:69], off offset:512 nt
	global_load_dwordx4 v[74:77], v[70:71], off offset:16 nt
	global_load_dwordx4 v[78:81], v[70:71], off nt
	s_nop 0
	global_load_dwordx4 v[66:69], v[70:71], off offset:528 nt
	s_nop 0
	global_load_dwordx4 v[70:73], v[70:71], off offset:512 nt
	v_lshlrev_b64 v[136:137], 11, v[136:137]
	s_waitcnt vmcnt(15)
	v_pk_add_f32 v[64:65], v[64:65], v[122:123]
	v_pk_add_f32 v[62:63], v[62:63], v[120:121]
	s_waitcnt vmcnt(14)
	v_pk_add_f32 v[60:61], v[60:61], v[126:127]
	v_pk_add_f32 v[58:59], v[58:59], v[124:125]
	s_waitcnt vmcnt(13)
	v_pk_add_f32 v[56:57], v[56:57], v[130:131]
	v_pk_add_f32 v[54:55], v[54:55], v[128:129]
	s_waitcnt vmcnt(12)
	v_pk_add_f32 v[120:121], v[52:53], v[134:135]
	v_pk_add_f32 v[122:123], v[50:51], v[132:133]
	v_cvt_pk_bf16_f32 v50, v62, v63
	v_cvt_pk_bf16_f32 v51, v64, v65
	v_cvt_pk_bf16_f32 v52, v58, v59
	v_cvt_pk_bf16_f32 v53, v60, v61
	v_mul_f32_e32 v63, v63, v63
	v_mul_f32_e32 v65, v65, v65
	v_mul_f32_e32 v59, v59, v59
	v_mul_f32_e32 v61, v61, v61
	v_mul_f32_e32 v124, v55, v55
	v_mul_f32_e32 v125, v57, v57
	v_mul_f32_e32 v126, v123, v123
	v_mul_f32_e32 v127, v121, v121
	v_fmac_f32_e32 v63, v62, v62
	v_fmac_f32_e32 v65, v64, v64
	v_fmac_f32_e32 v59, v58, v58
	v_fmac_f32_e32 v61, v60, v60
	v_fmac_f32_e32 v124, v54, v54
	v_fmac_f32_e32 v125, v56, v56
	v_fmac_f32_e32 v126, v122, v122
	v_fmac_f32_e32 v127, v120, v120
	v_add_f32_e32 v58, v63, v65
	v_add_f32_e32 v59, v59, v61
	v_add_f32_e32 v60, v124, v125
	v_add_f32_e32 v61, v126, v127
	v_add_f32_e32 v58, v58, v59
	v_add_f32_e32 v59, v60, v61
	v_add_f32_e32 v60, v58, v59
	ds_bpermute_b32 v61, v192, v60
	v_lshl_add_u64 v[58:59], s[16:17], 0, v[136:137]
	v_lshl_add_u64 v[58:59], v[178:179], 1, v[58:59]
	global_store_dwordx4 v[58:59], v[50:53], off sc1
	s_waitcnt lgkmcnt(0)
	s_nop 0
	v_add_f32_e32 v50, v60, v61
	ds_bpermute_b32 v51, v191, v50
	v_cvt_pk_bf16_f32 v52, v54, v55
	v_cvt_pk_bf16_f32 v53, v56, v57
	v_cvt_pk_bf16_f32 v54, v122, v123
	v_cvt_pk_bf16_f32 v55, v120, v121
	global_store_dwordx4 v[58:59], v[52:55], off offset:256 sc1
	s_and_saveexec_b64 s[0:1], vcc
	s_cbranch_execz .LBB0_555
	v_lshl_or_b32 v52, v0, 4, s15
	s_waitcnt lgkmcnt(0)
	v_add_f32_e32 v50, v50, v51
	ds_write_b32 v52, v50 offset:2048

.LBB0_854:
	s_mov_b32 s29, -1
	s_ashr_i32 s39, s38, 31
	v_mbcnt_lo_u32_b32 v0, s29, 0
	v_mbcnt_hi_u32_b32 v0, s29, v0
	s_lshl_b32 s29, s40, 8
	s_add_i32 s29, s29, s85
	v_and_or_b32 v212, v0, 15, s29
	s_lshl_b64 s[38:39], s[38:39], 8
	v_lshrrev_b32_e32 v0, 1, v0
	v_and_b32_e32 v0, 56, v0
	s_or_b64 s[38:39], s[38:39], s[80:81]
	s_ashr_i32 s53, s52, 31
	v_lshl_add_u64 v[210:211], s[38:39], 0, v[0:1]
	s_lshl_b64 s[38:39], s[52:53], 25
	v_ashrrev_i32_e32 v213, 31, v212
	s_add_u32 s54, s83, s38
	v_lshlrev_b64 v[130:131], 10, v[212:213]
	s_addc_u32 s55, s84, s39
	v_lshl_add_u64 v[132:133], v[210:211], 0, v[130:131]
	v_lshl_add_u64 v[130:131], v[132:133], 1, s[54:55]
	global_load_dwordx4 v[190:193], v[130:131], off nt
	s_cmp_eq_u32 s52, 2
	s_cselect_b64 s[56:57], -1, 0
	s_cmp_lg_u32 s52, 2
	s_cselect_b64 s[40:41], -1, 0
	s_add_u32 s52, s54, 0x2000000
	s_addc_u32 s53, s55, 0
	s_and_b64 vcc, exec, s[56:57]
	v_lshl_add_u64 v[132:133], v[132:133], 1, s[52:53]
	s_cbranch_vccnz .LBB0_856
	global_load_dwordx4 v[158:161], v[132:133], off nt
.LBB0_856:
	global_load_dwordx4 v[186:189], v[130:131], off offset:256 nt
	v_cndmask_b32_e64 v0, 0, 1, s[40:41]
	v_cmp_ne_u32_e64 s[38:39], 1, v0
	s_andn2_b64 vcc, exec, s[40:41]
	s_cbranch_vccnz .LBB0_858
	global_load_dwordx4 v[154:157], v[132:133], off offset:256 nt
.LBB0_858:
	v_or_b32_e32 v218, 16, v212
	v_ashrrev_i32_e32 v219, 31, v218
	v_lshlrev_b64 v[130:131], 10, v[218:219]
	v_lshl_add_u64 v[130:131], v[130:131], 0, v[210:211]
	v_lshl_add_u64 v[132:133], v[130:131], 1, s[54:55]
	global_load_dwordx4 v[182:185], v[132:133], off nt
	s_and_b64 vcc, exec, s[38:39]
	v_lshl_add_u64 v[130:131], v[130:131], 1, s[52:53]
	s_cbranch_vccnz .LBB0_860
	global_load_dwordx4 v[150:153], v[130:131], off nt
.LBB0_860:
	global_load_dwordx4 v[178:181], v[132:133], off offset:256 nt
	s_and_b64 vcc, exec, s[38:39]
	s_cbranch_vccnz .LBB0_862
	global_load_dwordx4 v[146:149], v[130:131], off offset:256 nt
.LBB0_862:
	v_or_b32_e32 v216, 32, v212
	v_ashrrev_i32_e32 v217, 31, v216
	v_lshlrev_b64 v[130:131], 10, v[216:217]
	v_lshl_add_u64 v[130:131], v[130:131], 0, v[210:211]
	v_lshl_add_u64 v[132:133], v[130:131], 1, s[54:55]
	global_load_dwordx4 v[174:177], v[132:133], off nt
	s_and_b64 vcc, exec, s[38:39]
	v_lshl_add_u64 v[130:131], v[130:131], 1, s[52:53]
	s_cbranch_vccnz .LBB0_864
	global_load_dwordx4 v[142:145], v[130:131], off nt
.LBB0_864:
	global_load_dwordx4 v[170:173], v[132:133], off offset:256 nt
	s_and_b64 vcc, exec, s[38:39]
	s_cbranch_vccnz .LBB0_866
	global_load_dwordx4 v[138:141], v[130:131], off offset:256 nt
.LBB0_866:
	v_or_b32_e32 v214, 48, v212
	v_ashrrev_i32_e32 v215, 31, v214
	v_lshlrev_b64 v[130:131], 10, v[214:215]
	v_lshl_add_u64 v[132:133], v[130:131], 0, v[210:211]
	v_lshl_add_u64 v[130:131], v[132:133], 1, s[54:55]
	global_load_dwordx4 v[166:169], v[130:131], off nt
	s_and_b64 vcc, exec, s[38:39]
	v_lshl_add_u64 v[220:221], v[132:133], 1, s[52:53]
	s_cbranch_vccnz .LBB0_868
	global_load_dwordx4 v[134:137], v[220:221], off nt
.LBB0_868:
	global_load_dwordx4 v[162:165], v[130:131], off offset:256 nt
	s_and_b64 vcc, exec, s[38:39]
	s_cbranch_vccnz .LBB0_870
	global_load_dwordx4 v[130:133], v[220:221], off offset:256 nt

.LBB0_902:
	v_add_u32_e32 v218, 0x80, v212
	v_ashrrev_i32_e32 v219, 31, v218
	v_lshlrev_b64 v[162:163], 10, v[218:219]
	v_lshl_add_u64 v[162:163], v[162:163], 0, v[210:211]
	v_lshl_add_u64 v[164:165], v[162:163], 1, s[54:55]
	global_load_dwordx4 v[190:193], v[164:165], off nt
	s_and_b64 vcc, exec, s[38:39]
	v_lshl_add_u64 v[162:163], v[162:163], 1, s[52:53]
	s_cbranch_vccnz .LBB0_904
	global_load_dwordx4 v[158:161], v[162:163], off nt
.LBB0_904:
	global_load_dwordx4 v[186:189], v[164:165], off offset:256 nt
	s_and_b64 vcc, exec, s[38:39]
	s_cbranch_vccnz .LBB0_906
	global_load_dwordx4 v[154:157], v[162:163], off offset:256 nt
.LBB0_906:
	v_add_u32_e32 v216, 0x90, v212
	v_ashrrev_i32_e32 v217, 31, v216
	v_lshlrev_b64 v[162:163], 10, v[216:217]
	v_lshl_add_u64 v[162:163], v[162:163], 0, v[210:211]
	v_lshl_add_u64 v[164:165], v[162:163], 1, s[54:55]
	global_load_dwordx4 v[182:185], v[164:165], off nt
	s_and_b64 vcc, exec, s[38:39]
	v_lshl_add_u64 v[162:163], v[162:163], 1, s[52:53]
	s_cbranch_vccnz .LBB0_908
	global_load_dwordx4 v[150:153], v[162:163], off nt
.LBB0_908:
	global_load_dwordx4 v[178:181], v[164:165], off offset:256 nt
	s_and_b64 vcc, exec, s[38:39]
	s_cbranch_vccnz .LBB0_910
	global_load_dwordx4 v[146:149], v[162:163], off offset:256 nt
.LBB0_910:
	v_add_u32_e32 v214, 0xa0, v212
	v_ashrrev_i32_e32 v215, 31, v214
	v_lshlrev_b64 v[162:163], 10, v[214:215]
	v_lshl_add_u64 v[162:163], v[162:163], 0, v[210:211]
	v_lshl_add_u64 v[164:165], v[162:163], 1, s[54:55]
	global_load_dwordx4 v[174:177], v[164:165], off nt
	s_and_b64 vcc, exec, s[38:39]
	v_lshl_add_u64 v[162:163], v[162:163], 1, s[52:53]
	s_cbranch_vccnz .LBB0_912
	global_load_dwordx4 v[142:145], v[162:163], off nt
.LBB0_912:
	global_load_dwordx4 v[170:173], v[164:165], off offset:256 nt
	s_and_b64 vcc, exec, s[38:39]
	s_cbranch_vccnz .LBB0_914
	global_load_dwordx4 v[138:141], v[162:163], off offset:256 nt
.LBB0_914:
	v_add_u32_e32 v212, 0xb0, v212
	v_ashrrev_i32_e32 v213, 31, v212
	v_lshlrev_b64 v[162:163], 10, v[212:213]
	v_lshl_add_u64 v[164:165], v[162:163], 0, v[210:211]
	v_lshl_add_u64 v[162:163], v[164:165], 1, s[54:55]
	global_load_dwordx4 v[166:169], v[162:163], off nt
	s_and_b64 vcc, exec, s[38:39]
	v_lshl_add_u64 v[220:221], v[164:165], 1, s[52:53]
	s_cbranch_vccnz .LBB0_916
	global_load_dwordx4 v[134:137], v[220:221], off nt
.LBB0_916:
	s_nop 0
	global_load_dwordx4 v[162:165], v[162:163], off offset:256 nt
	s_and_b64 vcc, exec, s[38:39]
	s_cbranch_vccnz .LBB0_918
	global_load_dwordx4 v[130:133], v[220:221], off offset:256 nt

.LBB0_1989:
	s_and_b64 vcc, exec, s[0:1]
	s_cbranch_vccz .LBB0_2111
	v_readlane_b32 s0, v253, 45
	s_cmp_eq_u32 s0, 0
	s_cbranch_scc0 .LBB0_2111
	v_readlane_b32 s0, v253, 41
	v_readlane_b32 s1, v253, 42
	s_andn2_b64 vcc, exec, s[0:1]
	s_cbranch_vccnz .LBB0_1995
	s_abs_i32 s1, s30
	s_mul_hi_u32 s14, s1, s27
	s_mul_i32 s14, s14, s33
	s_sub_i32 s1, s1, s14
	s_ashr_i32 s0, s30, 31
	s_sub_i32 s14, s1, s33
	s_cmp_ge_u32 s1, s33
	s_cselect_b32 s1, s14, s1
	s_sub_i32 s14, s1, s33
	s_cmp_ge_u32 s1, s33
	s_cselect_b32 s1, s14, s1
	s_xor_b32 s1, s1, s0
	s_sub_i32 s0, s1, s0
	s_ashr_i32 s1, s0, 31
	s_and_b32 s1, s1, s72
	s_add_i32 s0, s1, s0
	s_cmpk_gt_i32 s0, 0x57f
	s_cbranch_scc1 .LBB0_1994
	v_readlane_b32 s14, v253, 32
	s_lshl_b32 s14, s14, 14
	s_lshl_b64 s[16:17], s[86:87], 3
	v_readlane_b32 s34, v250, 3
	v_readlane_b32 s35, v250, 4
	s_add_u32 s16, s34, s16
	s_addc_u32 s17, s35, s17
	s_load_dwordx2 s[16:17], s[16:17], 0x90
	v_readlane_b32 s15, v253, 33
	v_readlane_b32 s15, v253, 38
	s_mul_hi_u32 s1, s15, 0xb00000
	s_mul_i32 s15, s15, 0xb00000
	s_waitcnt lgkmcnt(0)
	s_add_u32 s15, s16, s15
	s_addc_u32 s17, s17, s1
	s_ashr_i32 s1, s0, 31
	s_lshr_b32 s1, s1, 27
	s_add_i32 s1, s0, s1
	s_ashr_i32 s1, s1, 5
	s_lshl_b32 s16, s1, 6
	s_lshl_b32 s1, s1, 10
	s_lshl_b32 s0, s0, 5
	s_sub_i32 s0, s0, s1
	s_ashr_i32 s1, s0, 31
	s_waitcnt vmcnt(0)
	v_lshrrev_b32_e32 v35, 3, v198
	s_lshl_b64 s[34:35], s[0:1], 2
	s_waitcnt vmcnt(0)
	v_or_b32_e32 v30, s16, v35
	s_add_u32 s34, s15, s34
	v_lshlrev_b32_e32 v0, 4, v198
	s_addc_u32 s35, s17, s35
	v_and_b32_e32 v0, 0x70, v0
	v_ashrrev_i32_e32 v31, 31, v30
	v_or_b32_e32 v6, 8, v30
	v_lshl_add_u64 v[32:33], s[34:35], 0, v[0:1]
	v_lshlrev_b64 v[2:3], 12, v[30:31]
	v_ashrrev_i32_e32 v7, 31, v6
	v_lshl_add_u64 v[2:3], v[32:33], 0, v[2:3]
	v_lshlrev_b64 v[6:7], 12, v[6:7]
	v_or_b32_e32 v10, 16, v30
	global_load_dwordx4 v[2:5], v[2:3], off nt
	v_lshl_add_u64 v[6:7], v[32:33], 0, v[6:7]
	v_ashrrev_i32_e32 v11, 31, v10
	global_load_dwordx4 v[6:9], v[6:7], off nt
	v_lshlrev_b64 v[10:11], 12, v[10:11]
	v_or_b32_e32 v14, 24, v30
	v_lshl_add_u64 v[10:11], v[32:33], 0, v[10:11]
	v_ashrrev_i32_e32 v15, 31, v14
	global_load_dwordx4 v[10:13], v[10:11], off nt
	v_lshlrev_b64 v[14:15], 12, v[14:15]
	v_or_b32_e32 v18, 32, v30
	v_lshl_add_u64 v[14:15], v[32:33], 0, v[14:15]
	v_ashrrev_i32_e32 v19, 31, v18
	global_load_dwordx4 v[14:17], v[14:15], off nt
	v_lshlrev_b64 v[18:19], 12, v[18:19]
	v_or_b32_e32 v22, 40, v30
	v_lshl_add_u64 v[18:19], v[32:33], 0, v[18:19]
	v_ashrrev_i32_e32 v23, 31, v22
	global_load_dwordx4 v[18:21], v[18:19], off nt
	v_lshlrev_b64 v[22:23], 12, v[22:23]
	v_or_b32_e32 v26, 48, v30
	v_lshl_add_u64 v[22:23], v[32:33], 0, v[22:23]
	v_ashrrev_i32_e32 v27, 31, v26
	global_load_dwordx4 v[22:25], v[22:23], off nt
	v_lshlrev_b64 v[26:27], 12, v[26:27]
	v_or_b32_e32 v30, 56, v30
	v_lshl_add_u64 v[26:27], v[32:33], 0, v[26:27]
	v_ashrrev_i32_e32 v31, 31, v30
	global_load_dwordx4 v[26:29], v[26:27], off nt
	v_lshlrev_b64 v[30:31], 12, v[30:31]
	v_lshl_add_u64 v[30:31], v[32:33], 0, v[30:31]
	global_load_dwordx4 v[30:33], v[30:31], off nt
	s_mul_hi_i32 s1, s0, 0x1600
	s_mulk_i32 s0, 0x1600
	s_add_u32 s15, s74, s0
	s_addc_u32 s29, s75, s1
	s_ashr_i32 s17, s16, 31
	v_and_b32_e32 v0, 7, v235
	s_lshl_b64 s[0:1], s[16:17], 1
	v_lshlrev_b32_e32 v34, 4, v0
	s_add_u32 s0, s15, s0
	v_or_b32_e32 v36, s14, v34
	s_movk_i32 s15, 0x84
	v_mad_u32_u24 v36, v35, s15, v36
	v_mul_u32_u24_e32 v0, 0x420, v0
	s_addc_u32 s1, s29, s1
	s_waitcnt vmcnt(7)
	ds_write2_b32 v36, v2, v3 offset1:1
	ds_write2_b32 v36, v4, v5 offset0:2 offset1:3
	v_add_u32_e32 v2, 0x420, v36
	s_waitcnt vmcnt(6)
	ds_write2_b32 v2, v6, v7 offset1:1
	v_add_u32_e32 v2, 0x428, v36
	ds_write2_b32 v2, v8, v9 offset1:1
	v_add_u32_e32 v2, 0x840, v36
	s_waitcnt vmcnt(5)
	ds_write2_b32 v2, v10, v11 offset1:1
	v_add_u32_e32 v2, 0x848, v36
	ds_write2_b32 v2, v12, v13 offset1:1
	v_add_u32_e32 v2, 0xc60, v36
	s_waitcnt vmcnt(4)
	ds_write2_b32 v2, v14, v15 offset1:1
	v_add_u32_e32 v2, 0xc68, v36
	ds_write2_b32 v2, v16, v17 offset1:1
	v_add_u32_e32 v2, 0x1080, v36
	s_waitcnt vmcnt(3)
	ds_write2_b32 v2, v18, v19 offset1:1
	v_add_u32_e32 v2, 0x1088, v36
	ds_write2_b32 v2, v20, v21 offset1:1
	v_add_u32_e32 v2, 0x14a0, v36
	s_waitcnt vmcnt(2)
	ds_write2_b32 v2, v22, v23 offset1:1
	v_add_u32_e32 v2, 0x14a8, v36
	ds_write2_b32 v2, v24, v25 offset1:1
	v_add_u32_e32 v2, 0x18c0, v36
	s_waitcnt vmcnt(1)
	ds_write2_b32 v2, v26, v27 offset1:1
	v_add_u32_e32 v2, 0x18c8, v36
	ds_write2_b32 v2, v28, v29 offset1:1
	v_add_u32_e32 v2, 0x1ce0, v36
	s_waitcnt vmcnt(0)
	ds_write2_b32 v2, v30, v31 offset1:1
	v_add_u32_e32 v2, 0x1ce8, v36
	ds_write2_b32 v2, v32, v33 offset1:1
	s_waitcnt lgkmcnt(0)
	v_lshlrev_b32_e32 v2, 2, v35
	v_or3_b32 v26, s14, v0, v2
	v_mul_u32_u24_e32 v0, 0xb00, v35
	ds_read2_b32 v[6:7], v26 offset0:33 offset1:41
	ds_read2_b32 v[8:9], v26 offset1:8
	ds_read2_b32 v[10:11], v26 offset0:66 offset1:74
	ds_read2_b32 v[12:13], v26 offset0:99 offset1:107
	ds_read2_b32 v[14:15], v26 offset0:132 offset1:140
	ds_read2_b32 v[16:17], v26 offset0:165 offset1:173
	ds_read2_b32 v[18:19], v26 offset0:198 offset1:206
	ds_read2_b32 v[20:21], v26 offset0:231 offset1:239
	v_lshlrev_b32_e32 v0, 1, v0
	v_lshl_add_u64 v[22:23], s[0:1], 0, v[0:1]
	v_mov_b32_e32 v35, v1
	v_lshl_add_u64 v[22:23], v[22:23], 0, v[34:35]
	s_mov_b32 s0, 0x1c00000
	v_add_co_u32_e32 v24, vcc, s0, v22
	s_mov_b32 s0, 0x1c0b000
	s_nop 0
	v_addc_co_u32_e32 v25, vcc, 0, v23, vcc
	s_waitcnt lgkmcnt(6)
	v_cvt_pk_bf16_f32 v2, v8, v6
	s_waitcnt lgkmcnt(4)
	v_cvt_pk_bf16_f32 v3, v10, v12
	s_waitcnt lgkmcnt(2)
	v_cvt_pk_bf16_f32 v4, v14, v16
	s_waitcnt lgkmcnt(0)
	v_cvt_pk_bf16_f32 v5, v18, v20
	v_add_co_u32_e32 v6, vcc, s0, v22
	global_store_dwordx4 v[24:25], v[2:5], off sc1
	s_mov_b32 s0, 0x1c16000
	s_nop 0
	v_cvt_pk_bf16_f32 v2, v9, v7
	v_cvt_pk_bf16_f32 v3, v11, v13
	v_cvt_pk_bf16_f32 v4, v15, v17
	v_cvt_pk_bf16_f32 v5, v19, v21
	v_addc_co_u32_e32 v7, vcc, 0, v23, vcc
	global_store_dwordx4 v[6:7], v[2:5], off sc1
	ds_read2_b32 v[6:7], v26 offset0:49 offset1:57
	ds_read2_b32 v[8:9], v26 offset0:16 offset1:24
	ds_read2_b32 v[10:11], v26 offset0:82 offset1:90
	ds_read2_b32 v[12:13], v26 offset0:115 offset1:123
	ds_read2_b32 v[14:15], v26 offset0:148 offset1:156
	ds_read2_b32 v[16:17], v26 offset0:181 offset1:189
	ds_read2_b32 v[18:19], v26 offset0:214 offset1:222
	ds_read2_b32 v[20:21], v26 offset0:247 offset1:255
	v_add_co_u32_e32 v24, vcc, s0, v22
	s_waitcnt lgkmcnt(6)
	v_cvt_pk_bf16_f32 v2, v8, v6
	v_addc_co_u32_e32 v25, vcc, 0, v23, vcc
	s_waitcnt lgkmcnt(4)
	v_cvt_pk_bf16_f32 v3, v10, v12
	s_waitcnt lgkmcnt(2)
	v_cvt_pk_bf16_f32 v4, v14, v16
	s_waitcnt lgkmcnt(0)
	v_cvt_pk_bf16_f32 v5, v18, v20
	v_add_co_u32_e32 v6, vcc, 0x1c21000, v22
	global_store_dwordx4 v[24:25], v[2:5], off sc1
	s_nop 1
	v_cvt_pk_bf16_f32 v2, v9, v7
	v_cvt_pk_bf16_f32 v3, v11, v13
	v_cvt_pk_bf16_f32 v4, v15, v17
	v_cvt_pk_bf16_f32 v5, v19, v21
	v_addc_co_u32_e32 v7, vcc, 0, v23, vcc
	global_store_dwordx4 v[6:7], v[2:5], off sc1
	s_waitcnt lgkmcnt(0)
